# attention: the 70 block-scaled fp8 MFMAs whose two E8M0 scales are both 1.0 issued as the plain v_mfma_f32_32x32x64_f8f6f4 (same fp8 operands, same f32 accumulation, bit-identical results)
# speedup vs baseline: 1.0115x; 1.0115x over previous
; #define ISSUE_L(t, so) do { const unsigned so_ = (unsigned)(so); \
;     if ((t) < NT) { const char* kb_ = Kh + KROWB(t); pg8::glds16_s(kb_, koff[0], ldsK + so_); pg8::glds16_s(kb_, koff[1], ldsK + so_ + 1024u); } \
;     if ((t) >= 1) { const char* vb_ = Vh + KROWB((t) - 1); pg8::glds16_s(vb_, voff[0], ldsV + so_); pg8::glds16_s(vb_, voff[1], ldsV + so_ + 1024u); } } while (0)
; #define PBAR() asm volatile("s_waitcnt lgkmcnt(0)\n\ts_barrier" ::: "memory")
; #define ISSUE_L(t, sl) do { \
;     if ((t) < NT) pg8::glds16_s(Kh + KROWB(t), koff, ldsK + (unsigned)(sl) * 8192u); \
;     if ((t) >= 1 && (t) <= NT) pg8::glds16_s((const char*)V8 + (size_t)((t) - 1) * 8192, voff, ldsV + (unsigned)(sl) * 8192u); } while (0)
; #define PBAR() asm volatile("s_waitcnt lgkmcnt(0)\n\ts_barrier" ::: "memory")
; #define PBAR_V3() asm volatile("s_waitcnt vmcnt(2) lgkmcnt(0)\n\ts_barrier" ::: "memory")
; __device__ __forceinline__ void attn_unit_f8(const bf16_t* __restrict__ Q, const bf16_t* __restrict__ Kb, const unsigned char* __restrict__ V8, bf16_t* __restrict__ O, ...
;     ...
;     ISSUE_L(2, si); si = NEXT3(si); PBAR();
;     QKT(0); PBAR_V3();
.LBB0_1299:
	s_cmp_lg_u32 0, -1
	v_and_b32_e32 v181, 63, v179
	s_cselect_b32 s0, 0, 0
	v_lshrrev_b32_e32 v0, 5, v181
	s_add_i32 s58, s55, s0
	s_and_b32 s0, s26, 0x3fffffc0
	v_lshlrev_b32_e32 v198, 6, v178
	v_lshlrev_b32_e32 v199, 1, v0
	s_lshl_b32 s0, s0, 2
	v_and_b32_e32 v3, 3, v2
	v_add_u32_e32 v200, 0, v198
	v_bitop3_b32 v2, v199, v2, 3 bitop3:0x78
	s_add_i32 s66, s0, 0
	v_lshl_add_u32 v149, v2, 4, v200
	v_bitop3_b32 v2, v199, v3, 1 bitop3:0x36
	s_cmpk_lt_u32 s26, 0x100
	v_lshlrev_b32_e32 v152, 7, v178
	v_lshl_add_u32 v150, v2, 4, v200
	s_cselect_b64 s[80:81], -1, 0
	s_cmpk_gt_u32 s26, 0xff
	s_mov_b64 s[0:1], -1
	v_cmp_gt_u32_e64 s[2:3], 32, v181
	v_add_u32_e32 v153, 0, v152
	v_lshl_add_u32 v151, v178, 2, s66
	s_cbranch_scc0 .LBB0_1327
	s_or_b32 s0, s84, 0x80
	s_ashr_i32 s1, s0, 31
	s_lshl_b64 s[0:1], s[0:1], 10
	s_add_u32 s0, s59, s0
	s_addc_u32 s1, s60, s1
	s_cmp_lg_u32 s56, -1
	s_cselect_b32 s12, s56, 0
	s_add_i32 s12, s12, s55
	s_addk_i32 s12, 0x4000
	s_mov_b32 m0, s12
	s_nop 0
	global_load_lds_dwordx4 v148, s[0:1]
	s_add_u32 s0, s82, 0x2000
	s_addc_u32 s1, s83, 0
	s_cmp_lg_u32 0, -1
	s_cselect_b32 s12, 0, 0
	s_add_i32 s12, s12, s55
	s_addk_i32 s12, 0x4000
	s_mov_b32 m0, s12
	s_nop 0
	global_load_lds_dwordx4 v147, s[0:1]
	s_lshl_b32 s0, s51, 2
	v_or_b32_e32 v2, s0, v199
	v_bfe_u32 v3, v179, 1, 3
	v_bitop3_b32 v2, v2, v3, 1 bitop3:0x36
	v_bitop3_b32 v4, s0, v3, v199 bitop3:0x36
	v_lshlrev_b32_e32 v203, 4, v2
	s_waitcnt lgkmcnt(0)
	s_barrier
	v_lshlrev_b32_e32 v202, 4, v4
	v_add_u32_e32 v35, v153, v203
	v_add_u32_e32 v34, v153, v202
	ds_read_b128 v[6:9], v35 offset:24576
	ds_read_b128 v[2:5], v34 offset:24576
	ds_read_b128 v[18:21], v34 offset:28672
	ds_read_b128 v[22:25], v35 offset:28672
	s_waitcnt vmcnt(0) lgkmcnt(2)
	v_mfma_f32_32x32x64_f8f6f4 v[2:17], v[2:9], v[154:161], v[82:97]
	v_mov_b32_e32 v170, v1
	v_mov_b32_e32 v174, v1
	v_mov_b32_e32 v171, v1
	v_mov_b32_e32 v175, v1
	v_mov_b32_e32 v172, v1
	v_mov_b32_e32 v176, v1
	v_mov_b32_e32 v173, v1
	v_mov_b32_e32 v177, v1
	s_mov_b32 s72, 0
	s_mov_b32 s28, 2
	s_mov_b32 s67, 1
	s_nop 8
	v_max_f32_e32 v36, v3, v3
	s_waitcnt lgkmcnt(0)
	v_mfma_f32_32x32x64_f8f6f4 v[18:33], v[18:25], v[154:161], v[82:97]
	v_max_f32_e32 v37, v2, v2
	v_max_f32_e32 v36, v37, v36
	s_waitcnt vmcnt(2) lgkmcnt(0)
	s_barrier
; #define ISSUE_L(t, so) do { const unsigned so_ = (unsigned)(so); \
;     if ((t) < NT) { const char* kb_ = Kh + KROWB(t); pg8::glds16_s(kb_, koff[0], ldsK + so_); pg8::glds16_s(kb_, koff[1], ldsK + so_ + 1024u); } \
;     if ((t) >= 1) { const char* vb_ = Vh + KROWB((t) - 1); pg8::glds16_s(vb_, voff[0], ldsV + so_); pg8::glds16_s(vb_, voff[1], ldsV + so_ + 1024u); } } while (0)
; #define PBAR() asm volatile("s_waitcnt lgkmcnt(0)\n\ts_barrier" ::: "memory")
; #define PBAR_V0() asm volatile("s_waitcnt vmcnt(0) lgkmcnt(0)\n\ts_barrier" ::: "memory")
; #define ISSUE_L(t, sl) do { \
;     if ((t) < NT) pg8::glds16_s(Kh + KROWB(t), koff, ldsK + (unsigned)(sl) * 8192u); \
;     if ((t) >= 1 && (t) <= NT) pg8::glds16_s((const char*)V8 + (size_t)((t) - 1) * 8192, voff, ldsV + (unsigned)(sl) * 8192u); } while (0)
; #define PBAR() asm volatile("s_waitcnt lgkmcnt(0)\n\ts_barrier" ::: "memory")
; #define PBAR_V0() asm volatile("s_waitcnt vmcnt(0) lgkmcnt(0)\n\ts_barrier" ::: "memory")
; #define PBAR_V3() asm volatile("s_waitcnt vmcnt(2) lgkmcnt(0)\n\ts_barrier" ::: "memory")
; __device__ __forceinline__ void attn_unit_f8(const bf16_t* __restrict__ Q, const bf16_t* __restrict__ Kb, const unsigned char* __restrict__ V8, bf16_t* __restrict__ O, ...
;     ...
;     YSOFT(true); PBAR();
;     __builtin_amdgcn_s_setprio(1); QKT(sx); PV8(sx); sx = NEXT3(sx); __builtin_amdgcn_s_setprio(0);
;     ISSUE_L(3, si); si = NEXT3(si); if (3 < NT) PBAR_V3(); else PBAR_V0();
	s_nop 15
	s_nop 1
	v_max3_f32 v38, v4, v5, v19
	v_max3_f32 v36, v36, v18, v20
	v_max3_f32 v37, v38, v8, v9
	v_max3_f32 v36, v36, v21, v6
	v_max3_f32 v37, v37, v24, v25
	v_max3_f32 v36, v36, v7, v22
	v_max3_f32 v37, v37, v12, v13
	v_max3_f32 v36, v36, v23, v10
	v_max3_f32 v36, v36, v11, v26
	v_max3_f32 v37, v37, v28, v29
	v_max3_f32 v36, v36, v27, v14
	v_max3_f32 v37, v37, v16, v17
	v_max3_f32 v36, v36, v15, v30
	v_max3_f32 v37, v37, v32, v33
	v_max3_f32 v36, v36, v31, v37
	v_mov_b32_e32 v37, v36
	s_nop 1
	v_permlane32_swap_b32_e32 v36, v37
	v_max_f32_e32 v37, v37, v37
	v_max_f32_e32 v36, v36, v36
	v_max_f32_e32 v36, v36, v37
	v_add_f32_e32 v201, 0xc0c00000, v36
	v_sub_f32_e32 v2, v2, v201
	v_sub_f32_e32 v18, v18, v201
	v_sub_f32_e32 v3, v3, v201
	v_sub_f32_e32 v19, v19, v201
	v_sub_f32_e32 v6, v6, v201
	v_sub_f32_e32 v22, v22, v201
	v_sub_f32_e32 v7, v7, v201
	v_sub_f32_e32 v23, v23, v201
	v_sub_f32_e32 v10, v10, v201
	v_sub_f32_e32 v26, v26, v201
	v_sub_f32_e32 v11, v11, v201
	v_sub_f32_e32 v27, v27, v201
	v_sub_f32_e32 v14, v14, v201
	v_sub_f32_e32 v30, v30, v201
	v_sub_f32_e32 v15, v15, v201
	v_sub_f32_e32 v31, v31, v201
	v_exp_f32_e32 v2, v2
	v_exp_f32_e32 v3, v3
	v_exp_f32_e32 v6, v6
	v_exp_f32_e32 v7, v7
	v_exp_f32_e32 v10, v10
	v_exp_f32_e32 v11, v11
	v_exp_f32_e32 v14, v14
	v_exp_f32_e32 v15, v15
	v_exp_f32_e32 v18, v18
	v_exp_f32_e32 v19, v19
	v_exp_f32_e32 v22, v22
	v_exp_f32_e32 v23, v23
	v_exp_f32_e32 v26, v26
	v_exp_f32_e32 v27, v27
	v_exp_f32_e32 v30, v30
	v_exp_f32_e32 v31, v31
	v_sub_f32_e32 v4, v4, v201
	v_sub_f32_e32 v20, v20, v201
	v_sub_f32_e32 v5, v5, v201
	v_sub_f32_e32 v21, v21, v201
	v_sub_f32_e32 v8, v8, v201
	v_sub_f32_e32 v24, v24, v201
	v_sub_f32_e32 v9, v9, v201
	v_sub_f32_e32 v25, v25, v201
	v_sub_f32_e32 v12, v12, v201
	v_sub_f32_e32 v28, v28, v201
	v_sub_f32_e32 v13, v13, v201
	v_sub_f32_e32 v29, v29, v201
	v_sub_f32_e32 v16, v16, v201
	v_sub_f32_e32 v32, v32, v201
	v_sub_f32_e32 v17, v17, v201
	v_sub_f32_e32 v33, v33, v201
	v_exp_f32_e32 v4, v4
	v_exp_f32_e32 v5, v5
	v_exp_f32_e32 v8, v8
	v_exp_f32_e32 v9, v9
	v_exp_f32_e32 v12, v12
	v_exp_f32_e32 v13, v13
	v_exp_f32_e32 v16, v16
	v_exp_f32_e32 v17, v17
	v_exp_f32_e32 v20, v20
	v_exp_f32_e32 v21, v21
	v_exp_f32_e32 v24, v24
	v_exp_f32_e32 v25, v25
	v_exp_f32_e32 v28, v28
	v_exp_f32_e32 v29, v29
	v_exp_f32_e32 v32, v32
	v_exp_f32_e32 v33, v33
	v_cvt_pk_fp8_f32 v170, v2, v3
	v_cvt_pk_fp8_f32 v174, v18, v19
	v_cvt_pk_fp8_f32 v171, v6, v7
	v_cvt_pk_fp8_f32 v175, v22, v23
	v_cvt_pk_fp8_f32 v172, v10, v11
	v_cvt_pk_fp8_f32 v176, v26, v27
	v_cvt_pk_fp8_f32 v173, v14, v15
	v_cvt_pk_fp8_f32 v177, v30, v31
	v_xor_b32_e32 v98, 0x80000000, v201
	v_mov_b32_e32 v99, v98
	v_mov_b32_e32 v100, v98
	v_mov_b32_e32 v101, v98
	v_mov_b32_e32 v102, v98
	v_mov_b32_e32 v103, v98
	v_mov_b32_e32 v104, v98
	v_mov_b32_e32 v105, v98
	v_mov_b32_e32 v106, v98
	v_mov_b32_e32 v107, v98
	v_mov_b32_e32 v108, v98
	v_mov_b32_e32 v109, v98
	v_mov_b32_e32 v110, v98
	v_mov_b32_e32 v111, v98
	v_mov_b32_e32 v112, v98
	v_mov_b32_e32 v113, v98
	v_cvt_pk_fp8_f32 v170, v4, v5 op_sel:[0,0,1]
	v_cvt_pk_fp8_f32 v174, v20, v21 op_sel:[0,0,1]
	v_cvt_pk_fp8_f32 v171, v8, v9 op_sel:[0,0,1]
	v_cvt_pk_fp8_f32 v175, v24, v25 op_sel:[0,0,1]
	v_cvt_pk_fp8_f32 v172, v12, v13 op_sel:[0,0,1]
	v_cvt_pk_fp8_f32 v176, v28, v29 op_sel:[0,0,1]
	v_cvt_pk_fp8_f32 v173, v16, v17 op_sel:[0,0,1]
	v_cvt_pk_fp8_f32 v177, v32, v33 op_sel:[0,0,1]
	s_waitcnt lgkmcnt(0)
	s_barrier
	s_setprio 1
	ds_read_b128 v[6:9], v35 offset:32768
	ds_read_b128 v[2:5], v34 offset:32768
	ds_read_b128 v[66:69], v34 offset:36864
	ds_read_b128 v[70:73], v35 offset:36864
	v_mov_b64_e32 v[144:145], v[112:113]
	v_mov_b64_e32 v[142:143], v[110:111]
	s_waitcnt lgkmcnt(2)
	v_mfma_f32_32x32x64_f8f6f4 v[114:129], v[2:9], v[154:161], v[98:113]
	ds_read_b128 v[6:9], v150 offset:8192
	ds_read_b128 v[2:5], v149 offset:8192
	ds_read_b128 v[18:21], v149 offset:10240
	ds_read_b128 v[22:25], v150 offset:10240
	ds_read_b128 v[38:41], v150 offset:12288
	ds_read_b128 v[34:37], v149 offset:12288
	ds_read_b128 v[50:53], v149 offset:14336
	ds_read_b128 v[54:57], v150 offset:14336
	v_mov_b64_e32 v[140:141], v[108:109]
	v_mov_b64_e32 v[138:139], v[106:107]
	v_mov_b64_e32 v[136:137], v[104:105]
	v_mov_b64_e32 v[134:135], v[102:103]
	v_mov_b64_e32 v[132:133], v[100:101]
	v_mov_b64_e32 v[130:131], v[98:99]
	s_waitcnt lgkmcnt(6)
	v_mfma_f32_32x32x64_f8f6f4 v[2:17], v[170:177], v[2:9], 0
	s_waitcnt lgkmcnt(4)
	v_mfma_f32_32x32x64_f8f6f4 v[18:33], v[170:177], v[18:25], 0
	s_waitcnt lgkmcnt(2)
	v_mfma_f32_32x32x64_f8f6f4 v[34:49], v[170:177], v[34:41], 0
	s_waitcnt lgkmcnt(0)
	v_mfma_f32_32x32x64_f8f6f4 v[50:65], v[170:177], v[50:57], 0
	v_mfma_f32_32x32x64_f8f6f4 v[130:145], v[66:73], v[154:161], v[130:145]
	v_mfma_f32_32x32x64_f8f6f4 v[66:81], v[170:177], v[162:169], 0
	s_setprio 0
	s_or_b32 s0, s84, 0xc0
	s_ashr_i32 s1, s0, 31
	s_lshl_b64 s[0:1], s[0:1], 10
	s_add_u32 s0, s59, s0
	s_addc_u32 s1, s60, s1
	s_mov_b32 m0, s57
	s_nop 0
	global_load_lds_dwordx4 v148, s[0:1]
	s_add_u32 s0, s82, 0x4000
	s_addc_u32 s1, s83, 0
	s_mov_b32 m0, s58
	s_nop 0
	global_load_lds_dwordx4 v147, s[0:1]
	s_waitcnt vmcnt(2) lgkmcnt(0)
	s_barrier
	s_add_i32 s47, s61, 0x800
	s_add_u32 s26, s22, s65
	v_lshlrev_b32_e32 v204, 4, v0
	s_addc_u32 s27, s23, s64
	s_branch .LBB0_1304

; #define ISSUE_L(t, so) do { const unsigned so_ = (unsigned)(so); \
;     if ((t) < NT) { const char* kb_ = Kh + KROWB(t); pg8::glds16_s(kb_, koff[0], ldsK + so_); pg8::glds16_s(kb_, koff[1], ldsK + so_ + 1024u); } \
;     if ((t) >= 1) { const char* vb_ = Vh + KROWB((t) - 1); pg8::glds16_s(vb_, voff[0], ldsV + so_); pg8::glds16_s(vb_, voff[1], ldsV + so_ + 1024u); } } while (0)
; #define PBAR() asm volatile("s_waitcnt lgkmcnt(0)\n\ts_barrier" ::: "memory")
; #define PBAR_V0() asm volatile("s_waitcnt vmcnt(0) lgkmcnt(0)\n\ts_barrier" ::: "memory")
; #define YPH() YSOFT(false)
; #define ISSUE_L(t, sl) do { \
;     if ((t) < NT) pg8::glds16_s(Kh + KROWB(t), koff, ldsK + (unsigned)(sl) * 8192u); \
;     if ((t) >= 1 && (t) <= NT) pg8::glds16_s((const char*)V8 + (size_t)((t) - 1) * 8192, voff, ldsV + (unsigned)(sl) * 8192u); } while (0)
; #define PBAR() asm volatile("s_waitcnt lgkmcnt(0)\n\ts_barrier" ::: "memory")
; #define PBAR_V0() asm volatile("s_waitcnt vmcnt(0) lgkmcnt(0)\n\ts_barrier" ::: "memory")
; #define PBAR_V3() asm volatile("s_waitcnt vmcnt(2) lgkmcnt(0)\n\ts_barrier" ::: "memory")
; #define YPH() YSOFT(false)
; __device__ __forceinline__ void attn_unit_f8(const bf16_t* __restrict__ Q, const bf16_t* __restrict__ Kb, const unsigned char* __restrict__ V8, bf16_t* __restrict__ O, ...
;     ...
;     for (int t = 2; t < NT; ++t) {
;       YPH(); PBAR();
;       __builtin_amdgcn_s_setprio(1); QKT(sx); PV8(sx); sx = NEXT3(sx);
;       if (t + 2 <= NT) { ISSUE_L(t + 2, si); si = NEXT3(si); }
;       __builtin_amdgcn_s_setprio(0);
;       if (t + 2 < NT) PBAR_V3(); else PBAR_V0();
;     }
.LBB0_1303:
	v_exp_f32_e32 v114, v114
	v_exp_f32_e32 v115, v115
	v_exp_f32_e32 v118, v118
	v_exp_f32_e32 v119, v119
	v_exp_f32_e32 v122, v122
	v_exp_f32_e32 v123, v123
	v_exp_f32_e32 v126, v126
	v_exp_f32_e32 v127, v127
	v_exp_f32_e32 v130, v130
	v_exp_f32_e32 v131, v131
	v_exp_f32_e32 v134, v134
	v_exp_f32_e32 v135, v135
	v_exp_f32_e32 v138, v138
	v_exp_f32_e32 v139, v139
	v_exp_f32_e32 v142, v142
	v_exp_f32_e32 v143, v143
	v_exp_f32_e32 v116, v116
	v_exp_f32_e32 v117, v117
	v_exp_f32_e32 v120, v120
	v_exp_f32_e32 v121, v121
	v_exp_f32_e32 v124, v124
	v_exp_f32_e32 v125, v125
	v_exp_f32_e32 v128, v128
	v_exp_f32_e32 v129, v129
	v_exp_f32_e32 v132, v132
	v_exp_f32_e32 v133, v133
	v_exp_f32_e32 v136, v136
	v_exp_f32_e32 v137, v137
	v_exp_f32_e32 v140, v140
	v_exp_f32_e32 v141, v141
	v_exp_f32_e32 v144, v144
	v_exp_f32_e32 v145, v145
	v_cvt_pk_fp8_f32 v170, v114, v115
	v_cvt_pk_fp8_f32 v174, v130, v131
	v_cvt_pk_fp8_f32 v171, v118, v119
	v_cvt_pk_fp8_f32 v175, v134, v135
	v_cvt_pk_fp8_f32 v172, v122, v123
	v_cvt_pk_fp8_f32 v176, v138, v139
	v_cvt_pk_fp8_f32 v173, v126, v127
	v_cvt_pk_fp8_f32 v177, v142, v143
	v_cvt_pk_fp8_f32 v170, v116, v117 op_sel:[0,0,1]
	v_cvt_pk_fp8_f32 v174, v132, v133 op_sel:[0,0,1]
	v_cvt_pk_fp8_f32 v171, v120, v121 op_sel:[0,0,1]
	v_cvt_pk_fp8_f32 v175, v136, v137 op_sel:[0,0,1]
	v_cvt_pk_fp8_f32 v172, v124, v125 op_sel:[0,0,1]
	v_cvt_pk_fp8_f32 v176, v140, v141 op_sel:[0,0,1]
	v_cvt_pk_fp8_f32 v173, v128, v129 op_sel:[0,0,1]
	v_cvt_pk_fp8_f32 v177, v144, v145 op_sel:[0,0,1]
	s_waitcnt lgkmcnt(0)
	s_barrier
	s_setprio 1
	s_lshl_b32 s0, s28, 13
	v_add_u32_e32 v114, s0, v153
	v_add_u32_e32 v139, v114, v203
	v_add_u32_e32 v138, v114, v202
	ds_read_b128 v[118:121], v139 offset:24576
	ds_read_b128 v[114:117], v138 offset:24576
	v_add_u32_e32 v141, s0, v150
	v_add_u32_e32 v140, s0, v149
	v_mfma_f32_32x32x64_f8f6f4 v[66:81], v[170:177], v[162:169], v[66:81]
	s_add_i32 s0, s28, 1
	s_cmp_lg_u32 s28, 2
	s_cselect_b32 s28, s0, 0
	s_add_i32 s0, s47, s72
	s_ashr_i32 s1, s0, 31
	s_lshl_b64 s[0:1], s[0:1], 10
	s_add_u32 s0, s59, s0
	s_addc_u32 s1, s60, s1
	s_lshl_b32 s12, s67, 13
	s_add_i32 s13, s12, s57
	s_add_u32 s26, s26, 0x2000
	s_addc_u32 s27, s27, 0
	s_add_i32 s12, s12, s58
	s_waitcnt lgkmcnt(0)
	v_mfma_f32_32x32x64_f8f6f4 v[114:129], v[114:121], v[154:161], v[98:113]
	ds_read_b128 v[134:137], v141
	ds_read_b128 v[130:133], v140
	s_waitcnt lgkmcnt(0)
	v_mfma_f32_32x32x64_f8f6f4 v[2:17], v[170:177], v[130:137], v[2:17]
	ds_read_b128 v[130:133], v140 offset:2048
	ds_read_b128 v[134:137], v141 offset:2048
	s_waitcnt lgkmcnt(0)
	v_mfma_f32_32x32x64_f8f6f4 v[18:33], v[170:177], v[130:137], v[18:33]
	ds_read_b128 v[134:137], v141 offset:4096
	ds_read_b128 v[130:133], v140 offset:4096
	s_waitcnt lgkmcnt(0)
	v_mfma_f32_32x32x64_f8f6f4 v[34:49], v[170:177], v[130:137], v[34:49]
	ds_read_b128 v[130:133], v140 offset:6144
	ds_read_b128 v[134:137], v141 offset:6144
	s_waitcnt lgkmcnt(0)
	v_mfma_f32_32x32x64_f8f6f4 v[50:65], v[170:177], v[130:137], v[50:65]
	ds_read_b128 v[130:133], v138 offset:28672
	ds_read_b128 v[134:137], v139 offset:28672
	s_waitcnt lgkmcnt(0)
	v_mfma_f32_32x32x64_f8f6f4 v[130:145], v[130:137], v[154:161], v[98:113]
	s_mov_b32 m0, s13
	s_nop 0
	global_load_lds_dwordx4 v148, s[0:1]
	s_mov_b32 m0, s12
	s_nop 0
	global_load_lds_dwordx4 v147, s[26:27]
	s_add_i32 s0, s67, 1
	s_cmp_lg_u32 s67, 2
	s_cselect_b32 s67, s0, 0
	s_setprio 0
	s_waitcnt vmcnt(2) lgkmcnt(0)
	s_barrier
	s_add_i32 s72, s72, 64
	s_cmpk_eq_i32 s72, 0x2000
	s_cbranch_scc1 .LBB0_1308

; #define ISSUE_L(t, so) do { const unsigned so_ = (unsigned)(so); \
;     if ((t) < NT) { const char* kb_ = Kh + KROWB(t); pg8::glds16_s(kb_, koff[0], ldsK + so_); pg8::glds16_s(kb_, koff[1], ldsK + so_ + 1024u); } \
;     if ((t) >= 1) { const char* vb_ = Vh + KROWB((t) - 1); pg8::glds16_s(vb_, voff[0], ldsV + so_); pg8::glds16_s(vb_, voff[1], ldsV + so_ + 1024u); } } while (0)
; #define PBAR() asm volatile("s_waitcnt lgkmcnt(0)\n\ts_barrier" ::: "memory")
; #define PBAR_V0() asm volatile("s_waitcnt vmcnt(0) lgkmcnt(0)\n\ts_barrier" ::: "memory")
; #define YPH() YSOFT(false)
; #define ISSUE_L(t, sl) do { \
;     if ((t) < NT) pg8::glds16_s(Kh + KROWB(t), koff, ldsK + (unsigned)(sl) * 8192u); \
;     if ((t) >= 1 && (t) <= NT) pg8::glds16_s((const char*)V8 + (size_t)((t) - 1) * 8192, voff, ldsV + (unsigned)(sl) * 8192u); } while (0)
; #define PBAR() asm volatile("s_waitcnt lgkmcnt(0)\n\ts_barrier" ::: "memory")
; #define PBAR_V0() asm volatile("s_waitcnt vmcnt(0) lgkmcnt(0)\n\ts_barrier" ::: "memory")
; #define PBAR_V3() asm volatile("s_waitcnt vmcnt(2) lgkmcnt(0)\n\ts_barrier" ::: "memory")
; #define YPH() YSOFT(false)
; __device__ __forceinline__ void attn_unit_f8(const bf16_t* __restrict__ Q, const bf16_t* __restrict__ Kb, const unsigned char* __restrict__ V8, bf16_t* __restrict__ O, ...
;     ...
;   f32x16 p0, p1; i32x8 p8 = i32x8{};
;   i32x8 onesf = (i32x8){0x38383838, 0x38383838, 0x38383838, 0x38383838, 0x38383838, 0x38383838, 0x38383838, 0x38383838}; asm volatile("" : "+v"(onesf));
;   f32x16 negm = f32x16{}; asm volatile("" : "+v"(negm));
;   const int scl1 = 0x7F7F7F7F;
;     ...
;     for (int t = 2; t < NT; ++t) {
;       YPH(); PBAR();
;       __builtin_amdgcn_s_setprio(1); QKT(sx); PV8(sx); sx = NEXT3(sx);
;       if (t + 2 <= NT) { ISSUE_L(t + 2, si); si = NEXT3(si); }
;       __builtin_amdgcn_s_setprio(0);
;       if (t + 2 < NT) PBAR_V3(); else PBAR_V0();
;     }
;     YPH(); PBAR();
.LBB0_1314:
	v_exp_f32_e32 v114, v114
	v_exp_f32_e32 v115, v115
	v_exp_f32_e32 v118, v118
	v_exp_f32_e32 v119, v119
	v_exp_f32_e32 v122, v122
	v_exp_f32_e32 v123, v123
	v_exp_f32_e32 v126, v126
	v_exp_f32_e32 v127, v127
	v_exp_f32_e32 v130, v130
	v_exp_f32_e32 v131, v131
	v_exp_f32_e32 v134, v134
	v_exp_f32_e32 v135, v135
	v_exp_f32_e32 v138, v138
	v_exp_f32_e32 v139, v139
	v_exp_f32_e32 v142, v142
	v_exp_f32_e32 v143, v143
	v_exp_f32_e32 v116, v116
	v_exp_f32_e32 v117, v117
	v_exp_f32_e32 v120, v120
	v_exp_f32_e32 v121, v121
	v_exp_f32_e32 v124, v124
	v_exp_f32_e32 v125, v125
	v_exp_f32_e32 v128, v128
	v_exp_f32_e32 v129, v129
	v_exp_f32_e32 v132, v132
	v_exp_f32_e32 v133, v133
	v_exp_f32_e32 v136, v136
	v_exp_f32_e32 v137, v137
	v_exp_f32_e32 v140, v140
	v_exp_f32_e32 v141, v141
	v_exp_f32_e32 v144, v144
	v_exp_f32_e32 v145, v145
	v_cvt_pk_fp8_f32 v170, v114, v115
	v_cvt_pk_fp8_f32 v174, v130, v131
	v_cvt_pk_fp8_f32 v171, v118, v119
	v_cvt_pk_fp8_f32 v175, v134, v135
	v_cvt_pk_fp8_f32 v172, v122, v123
	v_cvt_pk_fp8_f32 v176, v138, v139
	v_cvt_pk_fp8_f32 v173, v126, v127
	v_cvt_pk_fp8_f32 v177, v142, v143
	v_cvt_pk_fp8_f32 v170, v116, v117 op_sel:[0,0,1]
	v_cvt_pk_fp8_f32 v174, v132, v133 op_sel:[0,0,1]
	v_cvt_pk_fp8_f32 v171, v120, v121 op_sel:[0,0,1]
	v_cvt_pk_fp8_f32 v175, v136, v137 op_sel:[0,0,1]
	v_cvt_pk_fp8_f32 v172, v124, v125 op_sel:[0,0,1]
	v_cvt_pk_fp8_f32 v176, v140, v141 op_sel:[0,0,1]
	v_cvt_pk_fp8_f32 v173, v128, v129 op_sel:[0,0,1]
	v_cvt_pk_fp8_f32 v177, v144, v145 op_sel:[0,0,1]
	s_waitcnt lgkmcnt(0)
	s_barrier
	s_setprio 1
	s_lshl_b32 s0, s28, 13
	s_add_i32 s1, s0, 0
	v_add_u32_e32 v114, s1, v152
	v_add_u32_e32 v139, v114, v203
	v_add_u32_e32 v138, v114, v202
	ds_read_b128 v[118:121], v139 offset:24576
	ds_read_b128 v[114:117], v138 offset:24576
	v_add_u32_e32 v141, s0, v150
	v_add_u32_e32 v140, s0, v149
	v_mfma_f32_32x32x64_f8f6f4 v[66:81], v[170:177], v[162:169], v[66:81]
	s_lshl_b32 s12, s67, 13
	s_add_u32 s0, s82, 0x106000
	s_addc_u32 s1, s83, 0
	s_add_i32 s12, s12, s58
	s_waitcnt lgkmcnt(0)
	v_mfma_f32_32x32x64_f8f6f4 v[114:129], v[114:121], v[154:161], v[98:113]
	ds_read_b128 v[134:137], v141
	ds_read_b128 v[130:133], v140
	s_waitcnt lgkmcnt(0)
	v_mfma_f32_32x32x64_f8f6f4 v[2:17], v[170:177], v[130:137], v[2:17]
	ds_read_b128 v[130:133], v140 offset:2048
	ds_read_b128 v[134:137], v141 offset:2048
	s_waitcnt lgkmcnt(0)
	v_mfma_f32_32x32x64_f8f6f4 v[18:33], v[170:177], v[130:137], v[18:33]
	ds_read_b128 v[134:137], v141 offset:4096
	ds_read_b128 v[130:133], v140 offset:4096
	s_waitcnt lgkmcnt(0)
	v_mfma_f32_32x32x64_f8f6f4 v[34:49], v[170:177], v[130:137], v[34:49]
	ds_read_b128 v[130:133], v140 offset:6144
	ds_read_b128 v[134:137], v141 offset:6144
	s_waitcnt lgkmcnt(0)
	v_mfma_f32_32x32x64_f8f6f4 v[50:65], v[170:177], v[130:137], v[50:65]
	ds_read_b128 v[130:133], v138 offset:28672
	ds_read_b128 v[134:137], v139 offset:28672
	s_waitcnt lgkmcnt(0)
	v_mfma_f32_32x32x64_f8f6f4 v[130:145], v[130:137], v[154:161], v[98:113]
	s_mov_b32 m0, s12
	s_nop 0
	global_load_lds_dwordx4 v147, s[0:1]
	s_setprio 0
	v_max_f32_e32 v205, v115, v115
	v_max_f32_e32 v206, v114, v114
	v_max_f32_e32 v205, v206, v205
	s_nop 15
	v_max3_f32 v206, v116, v117, v131
	v_max3_f32 v205, v205, v130, v132
	v_max3_f32 v205, v205, v133, v118
	v_max3_f32 v206, v206, v120, v121
	v_max3_f32 v205, v205, v119, v134
	v_max3_f32 v206, v206, v136, v137
	v_max3_f32 v205, v205, v135, v122
	v_max3_f32 v206, v206, v124, v125
	v_max3_f32 v205, v205, v123, v138
	v_max3_f32 v206, v206, v140, v141
	v_max3_f32 v205, v205, v139, v126
	v_max3_f32 v206, v206, v128, v129
	v_max3_f32 v205, v205, v127, v142
	v_max3_f32 v206, v206, v144, v145
	v_max3_f32 v205, v205, v143, v206
	v_mov_b32_e32 v206, v205
	s_nop 1
	v_permlane32_swap_b32_e32 v205, v206
	s_waitcnt vmcnt(0) lgkmcnt(0)
	s_barrier
	v_max_f32_e32 v206, v206, v206
	v_max_f32_e32 v205, v205, v205
	v_max_f32_e32 v205, v205, v206
	v_cmp_lt_f32_e32 vcc, s69, v205
	s_cbranch_vccz .LBB0_1320
	v_add_f32_e32 v98, 0xc0c00000, v205
	v_max_f32_e32 v205, 0, v98
	v_exp_f32_e64 v206, -v205
	v_add_f32_e32 v201, v201, v205
	v_xor_b32_e32 v98, 0x80000000, v201
	v_mov_b32_e32 v99, v98
	v_mov_b32_e32 v100, v98
	v_mov_b32_e32 v101, v98
	v_mov_b32_e32 v102, v98
	v_mov_b32_e32 v103, v98
	v_mov_b32_e32 v104, v98
	v_mov_b32_e32 v105, v98
	v_mov_b32_e32 v106, v98
	v_mov_b32_e32 v107, v98
	v_mov_b32_e32 v108, v98
	v_mov_b32_e32 v109, v98
	v_mov_b32_e32 v110, v98
	v_mov_b32_e32 v111, v98
	v_mov_b32_e32 v112, v98
	v_mov_b32_e32 v113, v98
	v_cmp_gt_f32_e32 vcc, 1.0, v206
	s_cbranch_vccz .LBB0_1319
	s_and_saveexec_b64 s[0:1], s[2:3]
	ds_write_b32 v151, v206 offset:49280
	s_or_b64 exec, exec, s[0:1]
	s_waitcnt lgkmcnt(0)
	v_add_u32_e32 v218, s66, v204
	ds_read_b128 v[206:209], v218 offset:49376
	ds_read_b128 v[210:213], v218 offset:49344
	ds_read_b128 v[214:217], v218 offset:49312
	ds_read_b128 v[218:221], v218 offset:49280
	s_waitcnt lgkmcnt(3)
	v_pk_mul_f32 v[14:15], v[14:15], v[206:207]
	s_waitcnt lgkmcnt(2)
	v_pk_mul_f32 v[10:11], v[10:11], v[210:211]
	s_waitcnt lgkmcnt(1)
	v_pk_mul_f32 v[6:7], v[6:7], v[214:215]
	v_pk_mul_f32 v[16:17], v[16:17], v[208:209]
	v_pk_mul_f32 v[12:13], v[12:13], v[212:213]
	v_pk_mul_f32 v[8:9], v[8:9], v[216:217]
	s_waitcnt lgkmcnt(0)
	v_pk_mul_f32 v[4:5], v[4:5], v[220:221]
	v_pk_mul_f32 v[2:3], v[2:3], v[218:219]
	v_pk_mul_f32 v[30:31], v[30:31], v[206:207]
	v_pk_mul_f32 v[26:27], v[26:27], v[210:211]
	v_pk_mul_f32 v[22:23], v[22:23], v[214:215]
	v_pk_mul_f32 v[32:33], v[32:33], v[208:209]
	v_pk_mul_f32 v[28:29], v[28:29], v[212:213]
	v_pk_mul_f32 v[24:25], v[24:25], v[216:217]
	v_pk_mul_f32 v[20:21], v[20:21], v[220:221]
	v_pk_mul_f32 v[18:19], v[18:19], v[218:219]
	v_pk_mul_f32 v[46:47], v[46:47], v[206:207]
	v_pk_mul_f32 v[42:43], v[42:43], v[210:211]
	v_pk_mul_f32 v[38:39], v[38:39], v[214:215]
	v_pk_mul_f32 v[48:49], v[48:49], v[208:209]
	v_pk_mul_f32 v[44:45], v[44:45], v[212:213]
	v_pk_mul_f32 v[40:41], v[40:41], v[216:217]
	v_pk_mul_f32 v[36:37], v[36:37], v[220:221]
	v_pk_mul_f32 v[34:35], v[34:35], v[218:219]
	v_pk_mul_f32 v[62:63], v[62:63], v[206:207]
	v_pk_mul_f32 v[58:59], v[58:59], v[210:211]
	v_pk_mul_f32 v[54:55], v[54:55], v[214:215]
	v_pk_mul_f32 v[64:65], v[64:65], v[208:209]
	v_pk_mul_f32 v[60:61], v[60:61], v[212:213]
	v_pk_mul_f32 v[56:57], v[56:57], v[216:217]
	v_pk_mul_f32 v[52:53], v[52:53], v[220:221]
	v_pk_mul_f32 v[50:51], v[50:51], v[218:219]
	v_pk_mul_f32 v[78:79], v[78:79], v[206:207]
	v_pk_mul_f32 v[74:75], v[74:75], v[210:211]
	v_pk_mul_f32 v[70:71], v[70:71], v[214:215]
	v_pk_mul_f32 v[80:81], v[80:81], v[208:209]
	v_pk_mul_f32 v[76:77], v[76:77], v[212:213]
	v_pk_mul_f32 v[72:73], v[72:73], v[216:217]
	v_pk_mul_f32 v[68:69], v[68:69], v[220:221]
	v_pk_mul_f32 v[66:67], v[66:67], v[218:219]

; #define ISSUE_L(t, so) do { const unsigned so_ = (unsigned)(so); \
;     if ((t) < NT) { const char* kb_ = Kh + KROWB(t); pg8::glds16_s(kb_, koff[0], ldsK + so_); pg8::glds16_s(kb_, koff[1], ldsK + so_ + 1024u); } \
;     if ((t) >= 1) { const char* vb_ = Vh + KROWB((t) - 1); pg8::glds16_s(vb_, voff[0], ldsV + so_); pg8::glds16_s(vb_, voff[1], ldsV + so_ + 1024u); } } while (0)
; #define PBAR() asm volatile("s_waitcnt lgkmcnt(0)\n\ts_barrier" ::: "memory")
; #define PBAR_V0() asm volatile("s_waitcnt vmcnt(0) lgkmcnt(0)\n\ts_barrier" ::: "memory")
; #define YPH() YSOFT(false)
; #define ISSUE_L(t, sl) do { \
;     if ((t) < NT) pg8::glds16_s(Kh + KROWB(t), koff, ldsK + (unsigned)(sl) * 8192u); \
;     if ((t) >= 1 && (t) <= NT) pg8::glds16_s((const char*)V8 + (size_t)((t) - 1) * 8192, voff, ldsV + (unsigned)(sl) * 8192u); } while (0)
; #define PBAR() asm volatile("s_waitcnt lgkmcnt(0)\n\ts_barrier" ::: "memory")
; #define PBAR_V0() asm volatile("s_waitcnt vmcnt(0) lgkmcnt(0)\n\ts_barrier" ::: "memory")
; #define PBAR_V3() asm volatile("s_waitcnt vmcnt(2) lgkmcnt(0)\n\ts_barrier" ::: "memory")
; #define YPH() YSOFT(false)
; __device__ __forceinline__ void attn_unit_f8(const bf16_t* __restrict__ Q, const bf16_t* __restrict__ Kb, const unsigned char* __restrict__ V8, bf16_t* __restrict__ O, ...
;     ...
;   f32x16 p0, p1; i32x8 p8 = i32x8{};
;   i32x8 onesf = (i32x8){0x38383838, 0x38383838, 0x38383838, 0x38383838, 0x38383838, 0x38383838, 0x38383838, 0x38383838}; asm volatile("" : "+v"(onesf));
;   f32x16 negm = f32x16{}; asm volatile("" : "+v"(negm));
;   const int scl1 = 0x7F7F7F7F;
;     ...
;     for (int t = 2; t < NT; ++t) {
;       YPH(); PBAR();
;       __builtin_amdgcn_s_setprio(1); QKT(sx); PV8(sx); sx = NEXT3(sx);
;       if (t + 2 <= NT) { ISSUE_L(t + 2, si); si = NEXT3(si); }
;       __builtin_amdgcn_s_setprio(0);
;       if (t + 2 < NT) PBAR_V3(); else PBAR_V0();
;     }
;     YPH(); PBAR();
.LBB0_1320:
	v_exp_f32_e32 v114, v114
	v_exp_f32_e32 v115, v115
	v_exp_f32_e32 v118, v118
	v_exp_f32_e32 v119, v119
	v_exp_f32_e32 v122, v122
	v_exp_f32_e32 v123, v123
	v_exp_f32_e32 v126, v126
	v_exp_f32_e32 v127, v127
	v_exp_f32_e32 v130, v130
	v_exp_f32_e32 v131, v131
	v_exp_f32_e32 v134, v134
	v_exp_f32_e32 v135, v135
	v_exp_f32_e32 v138, v138
	v_exp_f32_e32 v139, v139
	v_exp_f32_e32 v142, v142
	v_exp_f32_e32 v143, v143
	v_exp_f32_e32 v116, v116
	v_exp_f32_e32 v117, v117
	v_exp_f32_e32 v120, v120
	v_exp_f32_e32 v121, v121
	v_exp_f32_e32 v124, v124
	v_exp_f32_e32 v125, v125
	v_exp_f32_e32 v128, v128
	v_exp_f32_e32 v129, v129
	v_exp_f32_e32 v132, v132
	v_exp_f32_e32 v133, v133
	v_exp_f32_e32 v136, v136
	v_exp_f32_e32 v137, v137
	v_exp_f32_e32 v140, v140
	v_exp_f32_e32 v141, v141
	v_exp_f32_e32 v144, v144
	v_exp_f32_e32 v145, v145
	v_cvt_pk_fp8_f32 v170, v114, v115
	v_cvt_pk_fp8_f32 v174, v130, v131
	v_cvt_pk_fp8_f32 v171, v118, v119
	v_cvt_pk_fp8_f32 v175, v134, v135
	v_cvt_pk_fp8_f32 v172, v122, v123
	v_cvt_pk_fp8_f32 v176, v138, v139
	v_cvt_pk_fp8_f32 v173, v126, v127
	v_cvt_pk_fp8_f32 v177, v142, v143
	v_cvt_pk_fp8_f32 v170, v116, v117 op_sel:[0,0,1]
	v_cvt_pk_fp8_f32 v174, v132, v133 op_sel:[0,0,1]
	v_cvt_pk_fp8_f32 v171, v120, v121 op_sel:[0,0,1]
	v_cvt_pk_fp8_f32 v175, v136, v137 op_sel:[0,0,1]
	v_cvt_pk_fp8_f32 v172, v124, v125 op_sel:[0,0,1]
	v_cvt_pk_fp8_f32 v176, v140, v141 op_sel:[0,0,1]
	v_cvt_pk_fp8_f32 v173, v128, v129 op_sel:[0,0,1]
	v_cvt_pk_fp8_f32 v177, v144, v145 op_sel:[0,0,1]
	s_add_i32 s0, s28, 1
	s_waitcnt lgkmcnt(0)
	s_barrier
	s_cmp_lg_u32 s28, 2
	s_cselect_b32 s26, s0, 0
	s_setprio 1
	s_lshl_b32 s27, s26, 13
	s_add_i32 s0, s27, 0
	v_add_u32_e32 v114, s0, v152
	v_add_u32_e32 v139, v114, v203
	v_add_u32_e32 v138, v114, v202
	ds_read_b128 v[118:121], v139 offset:24576
	ds_read_b128 v[114:117], v138 offset:24576
	v_add_u32_e32 v141, s27, v150
	v_add_u32_e32 v140, s27, v149
	v_mfma_f32_32x32x64_f8f6f4 v[66:81], v[170:177], v[162:169], v[66:81]
	s_waitcnt lgkmcnt(0)
	v_mfma_f32_32x32x64_f8f6f4 v[114:129], v[114:121], v[154:161], v[98:113]
	ds_read_b128 v[134:137], v141
	ds_read_b128 v[130:133], v140
	s_waitcnt lgkmcnt(0)
	v_mfma_f32_32x32x64_f8f6f4 v[2:17], v[170:177], v[130:137], v[2:17]
	ds_read_b128 v[130:133], v140 offset:2048
	ds_read_b128 v[134:137], v141 offset:2048
	s_waitcnt lgkmcnt(0)
	v_mfma_f32_32x32x64_f8f6f4 v[18:33], v[170:177], v[130:137], v[18:33]
	ds_read_b128 v[134:137], v141 offset:4096
	ds_read_b128 v[130:133], v140 offset:4096
	s_waitcnt lgkmcnt(0)
	v_mfma_f32_32x32x64_f8f6f4 v[34:49], v[170:177], v[130:137], v[34:49]
	ds_read_b128 v[130:133], v140 offset:6144
	ds_read_b128 v[134:137], v141 offset:6144
	s_waitcnt lgkmcnt(0)
	v_mfma_f32_32x32x64_f8f6f4 v[50:65], v[170:177], v[130:137], v[50:65]
	ds_read_b128 v[130:133], v138 offset:28672
	ds_read_b128 v[134:137], v139 offset:28672
	s_waitcnt lgkmcnt(0)
	v_mfma_f32_32x32x64_f8f6f4 v[98:113], v[130:137], v[154:161], v[98:113]
	s_setprio 0
	v_max_f32_e32 v130, v115, v115
	v_max_f32_e32 v131, v114, v114
	v_max_f32_e32 v130, v131, v130
	s_nop 15
	v_max3_f32 v131, v116, v117, v99
	v_max3_f32 v130, v130, v98, v100
	v_max3_f32 v130, v130, v101, v118
	v_max3_f32 v131, v131, v120, v121
	v_max3_f32 v130, v130, v119, v102
	v_max3_f32 v131, v131, v104, v105
	v_max3_f32 v130, v130, v103, v122
	v_max3_f32 v131, v131, v124, v125
	v_max3_f32 v130, v130, v123, v106
	v_max3_f32 v131, v131, v108, v109
	v_max3_f32 v130, v130, v107, v126
	v_max3_f32 v131, v131, v128, v129
	v_max3_f32 v130, v130, v127, v110
	v_max3_f32 v131, v131, v112, v113
	v_max3_f32 v130, v130, v111, v131
	v_mov_b32_e32 v131, v130
	s_nop 1
	v_permlane32_swap_b32_e32 v130, v131
	s_waitcnt vmcnt(0) lgkmcnt(0)
	s_barrier
	v_max_f32_e32 v131, v131, v131
	v_max_f32_e32 v130, v130, v130
	v_max_f32_e32 v130, v130, v131
	v_cmp_lt_f32_e32 vcc, s69, v130
	s_cbranch_vccz .LBB0_1326
	v_add_f32_e32 v130, 0xc0c00000, v130
	v_max_f32_e32 v202, 0, v130
	v_add_f32_e32 v130, v201, v202
	v_xor_b32_e32 v130, 0x80000000, v130
	v_mov_b32_e32 v131, v130
	v_mov_b32_e32 v132, v130
	v_mov_b32_e32 v133, v130
	v_mov_b32_e32 v134, v130
	v_mov_b32_e32 v135, v130
	v_mov_b32_e32 v136, v130
	v_mov_b32_e32 v137, v130
	v_mov_b32_e32 v138, v130
	v_mov_b32_e32 v139, v130
	v_mov_b32_e32 v140, v130
	v_mov_b32_e32 v141, v130
	v_mov_b32_e32 v142, v130
	v_mov_b32_e32 v143, v130
	v_mov_b32_e32 v144, v130
	v_mov_b32_e32 v145, v130
	s_nop 0
	v_exp_f32_e64 v130, -v202
	s_nop 0
	v_cmp_gt_f32_e32 vcc, 1.0, v130
	s_cbranch_vccz .LBB0_1325
	s_and_saveexec_b64 s[0:1], s[2:3]
	ds_write_b32 v151, v130 offset:49280
	s_or_b64 exec, exec, s[0:1]
	s_waitcnt lgkmcnt(0)
	v_add_u32_e32 v142, s66, v204
	ds_read_b128 v[130:133], v142 offset:49376
	ds_read_b128 v[134:137], v142 offset:49344
	ds_read_b128 v[138:141], v142 offset:49312
	ds_read_b128 v[142:145], v142 offset:49280
	s_waitcnt lgkmcnt(3)
	v_pk_mul_f32 v[14:15], v[14:15], v[130:131]
	s_waitcnt lgkmcnt(2)
	v_pk_mul_f32 v[10:11], v[10:11], v[134:135]
	s_waitcnt lgkmcnt(1)
	v_pk_mul_f32 v[6:7], v[6:7], v[138:139]
	v_pk_mul_f32 v[16:17], v[16:17], v[132:133]
	v_pk_mul_f32 v[12:13], v[12:13], v[136:137]
	v_pk_mul_f32 v[8:9], v[8:9], v[140:141]
	s_waitcnt lgkmcnt(0)
	v_pk_mul_f32 v[4:5], v[4:5], v[144:145]
	v_pk_mul_f32 v[2:3], v[2:3], v[142:143]
	v_pk_mul_f32 v[30:31], v[30:31], v[130:131]
	v_pk_mul_f32 v[26:27], v[26:27], v[134:135]
	v_pk_mul_f32 v[22:23], v[22:23], v[138:139]
	v_pk_mul_f32 v[32:33], v[32:33], v[132:133]
	v_pk_mul_f32 v[28:29], v[28:29], v[136:137]
	v_pk_mul_f32 v[24:25], v[24:25], v[140:141]
	v_pk_mul_f32 v[20:21], v[20:21], v[144:145]
	v_pk_mul_f32 v[18:19], v[18:19], v[142:143]
	v_pk_mul_f32 v[46:47], v[46:47], v[130:131]
	v_pk_mul_f32 v[42:43], v[42:43], v[134:135]
	v_pk_mul_f32 v[38:39], v[38:39], v[138:139]
	v_pk_mul_f32 v[48:49], v[48:49], v[132:133]
	v_pk_mul_f32 v[44:45], v[44:45], v[136:137]
	v_pk_mul_f32 v[40:41], v[40:41], v[140:141]
	v_pk_mul_f32 v[36:37], v[36:37], v[144:145]
	v_pk_mul_f32 v[34:35], v[34:35], v[142:143]
	v_pk_mul_f32 v[62:63], v[62:63], v[130:131]
	v_pk_mul_f32 v[58:59], v[58:59], v[134:135]
	v_pk_mul_f32 v[54:55], v[54:55], v[138:139]
	v_pk_mul_f32 v[64:65], v[64:65], v[132:133]
	v_pk_mul_f32 v[60:61], v[60:61], v[136:137]
	v_pk_mul_f32 v[56:57], v[56:57], v[140:141]
	v_pk_mul_f32 v[52:53], v[52:53], v[144:145]
	v_pk_mul_f32 v[50:51], v[50:51], v[142:143]
	v_pk_mul_f32 v[78:79], v[78:79], v[130:131]
	v_pk_mul_f32 v[74:75], v[74:75], v[134:135]
	v_pk_mul_f32 v[70:71], v[70:71], v[138:139]
	v_pk_mul_f32 v[80:81], v[80:81], v[132:133]
	v_pk_mul_f32 v[76:77], v[76:77], v[136:137]
	v_pk_mul_f32 v[72:73], v[72:73], v[140:141]
	v_pk_mul_f32 v[68:69], v[68:69], v[144:145]
	v_pk_mul_f32 v[66:67], v[66:67], v[142:143]

; #define ISSUE_L(t, so) do { const unsigned so_ = (unsigned)(so); \
;     if ((t) < NT) { const char* kb_ = Kh + KROWB(t); pg8::glds16_s(kb_, koff[0], ldsK + so_); pg8::glds16_s(kb_, koff[1], ldsK + so_ + 1024u); } \
;     if ((t) >= 1) { const char* vb_ = Vh + KROWB((t) - 1); pg8::glds16_s(vb_, voff[0], ldsV + so_); pg8::glds16_s(vb_, voff[1], ldsV + so_ + 1024u); } } while (0)
; #define PBAR() asm volatile("s_waitcnt lgkmcnt(0)\n\ts_barrier" ::: "memory")
; #define PBAR_V0() asm volatile("s_waitcnt vmcnt(0) lgkmcnt(0)\n\ts_barrier" ::: "memory")
; #define YPH() YSOFT(false)
; #define ISSUE_L(t, sl) do { \
;     if ((t) < NT) pg8::glds16_s(Kh + KROWB(t), koff, ldsK + (unsigned)(sl) * 8192u); \
;     if ((t) >= 1 && (t) <= NT) pg8::glds16_s((const char*)V8 + (size_t)((t) - 1) * 8192, voff, ldsV + (unsigned)(sl) * 8192u); } while (0)
; #define PBAR() asm volatile("s_waitcnt lgkmcnt(0)\n\ts_barrier" ::: "memory")
; #define PBAR_V0() asm volatile("s_waitcnt vmcnt(0) lgkmcnt(0)\n\ts_barrier" ::: "memory")
; #define PBAR_V3() asm volatile("s_waitcnt vmcnt(2) lgkmcnt(0)\n\ts_barrier" ::: "memory")
; #define YPH() YSOFT(false)
; __device__ __forceinline__ void attn_unit_f8(const bf16_t* __restrict__ Q, const bf16_t* __restrict__ Kb, const unsigned char* __restrict__ V8, bf16_t* __restrict__ O, ...
;     ...
;   if (!pref_in) { ISSUE_L(0, 0); ISSUE_L(1, 1); PBAR_V3(); }
;   else PBAR_V0();
;   int sx = 1, si = 2;
;   if (cq == 0) {
;     QKT(0); ISSUE_L(2, si); si = NEXT3(si); PBAR();
;     YSOFT(true); PBAR_V3();
;     ...
;     YPH(); PBAR();
;     PV8(sx); PBAR();
.LBB0_1326:
	v_exp_f32_e32 v114, v114
	v_exp_f32_e32 v115, v115
	v_exp_f32_e32 v118, v118
	v_exp_f32_e32 v119, v119
	v_exp_f32_e32 v122, v122
	v_exp_f32_e32 v123, v123
	v_exp_f32_e32 v126, v126
	v_exp_f32_e32 v127, v127
	v_exp_f32_e32 v98, v98
	v_exp_f32_e32 v99, v99
	v_exp_f32_e32 v102, v102
	v_exp_f32_e32 v103, v103
	v_exp_f32_e32 v106, v106
	v_exp_f32_e32 v107, v107
	v_exp_f32_e32 v110, v110
	v_exp_f32_e32 v111, v111
	v_exp_f32_e32 v116, v116
	v_exp_f32_e32 v117, v117
	v_exp_f32_e32 v120, v120
	v_exp_f32_e32 v121, v121
	v_exp_f32_e32 v124, v124
	v_exp_f32_e32 v125, v125
	v_exp_f32_e32 v128, v128
	v_exp_f32_e32 v129, v129
	v_exp_f32_e32 v100, v100
	v_exp_f32_e32 v101, v101
	v_exp_f32_e32 v104, v104
	v_exp_f32_e32 v105, v105
	v_exp_f32_e32 v108, v108
	v_exp_f32_e32 v109, v109
	v_exp_f32_e32 v112, v112
	v_exp_f32_e32 v113, v113
	v_cvt_pk_fp8_f32 v170, v114, v115
	v_cvt_pk_fp8_f32 v174, v98, v99
	v_cvt_pk_fp8_f32 v171, v118, v119
	v_cvt_pk_fp8_f32 v175, v102, v103
	v_cvt_pk_fp8_f32 v172, v122, v123
	v_cvt_pk_fp8_f32 v176, v106, v107
	v_cvt_pk_fp8_f32 v173, v126, v127
	v_cvt_pk_fp8_f32 v177, v110, v111
	s_addk_i32 s27, 0x2000
	v_cvt_pk_fp8_f32 v170, v116, v117 op_sel:[0,0,1]
	v_cvt_pk_fp8_f32 v174, v100, v101 op_sel:[0,0,1]
	v_cvt_pk_fp8_f32 v171, v120, v121 op_sel:[0,0,1]
	v_cvt_pk_fp8_f32 v175, v104, v105 op_sel:[0,0,1]
	v_cvt_pk_fp8_f32 v172, v124, v125 op_sel:[0,0,1]
	v_cvt_pk_fp8_f32 v176, v108, v109 op_sel:[0,0,1]
	v_cvt_pk_fp8_f32 v173, v128, v129 op_sel:[0,0,1]
	v_cvt_pk_fp8_f32 v177, v112, v113 op_sel:[0,0,1]
	s_cmp_lg_u32 s26, 2
	s_cselect_b32 s0, s27, 0
	s_waitcnt lgkmcnt(0)
	s_barrier
	v_add_u32_e32 v115, s0, v150
	v_add_u32_e32 v114, s0, v149
	ds_read_b128 v[102:105], v115
	ds_read_b128 v[98:101], v114
	ds_read_b128 v[106:109], v114 offset:2048
	ds_read_b128 v[110:113], v115 offset:2048
	s_waitcnt lgkmcnt(2)
	v_mfma_f32_32x32x64_f8f6f4 v[2:17], v[170:177], v[98:105], v[2:17]
	s_mov_b64 s[0:1], 0
	s_waitcnt lgkmcnt(0)
	v_mfma_f32_32x32x64_f8f6f4 v[18:33], v[170:177], v[106:113], v[18:33]
	ds_read_b128 v[102:105], v115 offset:4096
	ds_read_b128 v[98:101], v114 offset:4096
	ds_read_b128 v[106:109], v114 offset:6144
	ds_read_b128 v[110:113], v115 offset:6144
	s_waitcnt lgkmcnt(0)
	s_barrier
	s_waitcnt lgkmcnt(2)
	v_mfma_f32_32x32x64_f8f6f4 v[34:49], v[170:177], v[98:105], v[34:49]
	s_waitcnt lgkmcnt(0)
	v_mfma_f32_32x32x64_f8f6f4 v[50:65], v[170:177], v[106:113], v[50:65]
	v_mfma_f32_32x32x64_f8f6f4 v[66:81], v[170:177], v[162:169], v[66:81]
.LBB0_1327:
	s_and_b64 vcc, exec, s[0:1]
	s_cbranch_vccz .LBB0_1355
	s_nop 5
	v_or_b32_e32 v2, 1, v199
	v_lshrrev_b32_e32 v4, 1, v179
	v_bitop3_b32 v2, v2, v4, 7 bitop3:0x78
	v_add_u32_e32 v3, v200, v198
	v_bitop3_b32 v5, v199, v4, 7 bitop3:0x78
	v_lshlrev_b32_e32 v140, 4, v2
	v_lshlrev_b32_e32 v139, 4, v5
	v_add_u32_e32 v27, v3, v140
	v_add_u32_e32 v26, v3, v139
	ds_read_b128 v[6:9], v27 offset:24576
	ds_read_b128 v[2:5], v26 offset:24576
	ds_read_b128 v[18:21], v26 offset:28672
	ds_read_b128 v[22:25], v27 offset:28672
	s_waitcnt vmcnt(0) lgkmcnt(2)
	v_mfma_f32_32x32x64_f8f6f4 v[2:17], v[2:9], v[154:161], v[82:97]
	s_or_b32 s0, s84, 0x80
	s_ashr_i32 s1, s0, 31
	s_lshl_b64 s[0:1], s[0:1], 10
	s_add_u32 s0, s59, s0
	s_addc_u32 s1, s60, s1
	s_cmp_lg_u32 s56, -1
	s_cselect_b32 s2, s56, 0
	s_add_i32 s2, s2, s55
	s_addk_i32 s2, 0x4000
	s_mov_b32 m0, s2
	s_nop 0
	global_load_lds_dwordx4 v148, s[0:1]
	s_add_u32 s0, s82, 0x2000
	v_mov_b32_e32 v130, v1
	v_mov_b32_e32 v134, v1
	v_mov_b32_e32 v131, v1
	v_mov_b32_e32 v135, v1
	s_waitcnt lgkmcnt(0)
	v_mfma_f32_32x32x64_f8f6f4 v[82:97], v[18:25], v[154:161], v[82:97]
	s_nop 3
	v_max_f32_e32 v18, v3, v3
	v_max_f32_e32 v19, v2, v2
	v_max_f32_e32 v18, v19, v18
	v_mov_b32_e32 v132, v1
	v_mov_b32_e32 v136, v1
	v_mov_b32_e32 v133, v1
	v_mov_b32_e32 v137, v1
	s_addc_u32 s1, s83, 0
	s_cmp_lg_u32 0, -1
	s_cselect_b32 s2, 0, 0
	s_add_i32 s2, s2, s55
	s_addk_i32 s2, 0x4000
	s_mov_b32 m0, s2
	s_nop 0
	global_load_lds_dwordx4 v147, s[0:1]
	s_waitcnt lgkmcnt(0)
	s_barrier
	v_lshlrev_b32_e32 v141, 2, v0
	s_nop 2
	v_max3_f32 v19, v4, v5, v83
	v_max3_f32 v18, v18, v82, v84
	v_max3_f32 v18, v18, v85, v6
	v_max3_f32 v19, v19, v8, v9
	v_max3_f32 v18, v18, v7, v86
	v_max3_f32 v19, v19, v88, v89
	v_max3_f32 v18, v18, v87, v10
	v_max3_f32 v19, v19, v12, v13
	v_max3_f32 v18, v18, v11, v90
	v_max3_f32 v19, v19, v92, v93
	v_max3_f32 v18, v18, v91, v14
	v_max3_f32 v19, v19, v16, v17
	v_max3_f32 v18, v18, v15, v94
	v_max3_f32 v19, v19, v96, v97
	v_max3_f32 v18, v18, v95, v19
	v_mov_b32_e32 v19, v18
	s_nop 1
	v_permlane32_swap_b32_e32 v18, v19
	v_max_f32_e32 v19, v19, v19
	v_max_f32_e32 v18, v18, v18
	v_max_f32_e32 v18, v18, v19
	v_add_f32_e32 v138, 0xc0c00000, v18
	v_sub_f32_e32 v2, v2, v138
	v_sub_f32_e32 v18, v82, v138
	v_sub_f32_e32 v3, v3, v138
	v_sub_f32_e32 v19, v83, v138
	v_sub_f32_e32 v6, v6, v138
	v_sub_f32_e32 v22, v86, v138
	v_sub_f32_e32 v7, v7, v138
	v_sub_f32_e32 v23, v87, v138
	v_sub_f32_e32 v10, v10, v138
	v_sub_f32_e32 v28, v90, v138
	v_sub_f32_e32 v11, v11, v138
	v_sub_f32_e32 v29, v91, v138
	v_sub_f32_e32 v14, v14, v138
	v_sub_f32_e32 v32, v94, v138
	v_sub_f32_e32 v15, v15, v138
	v_sub_f32_e32 v33, v95, v138
	v_exp_f32_e32 v2, v2
	v_exp_f32_e32 v3, v3
	v_exp_f32_e32 v6, v6
	v_exp_f32_e32 v7, v7
	v_exp_f32_e32 v10, v10
	v_exp_f32_e32 v11, v11
	v_exp_f32_e32 v14, v14
	v_exp_f32_e32 v15, v15
	v_exp_f32_e32 v18, v18
	v_exp_f32_e32 v19, v19
	v_exp_f32_e32 v22, v22
	v_exp_f32_e32 v23, v23
	v_exp_f32_e32 v28, v28
	v_exp_f32_e32 v29, v29
	v_exp_f32_e32 v32, v32
	v_exp_f32_e32 v33, v33
	v_sub_f32_e32 v4, v4, v138
	v_sub_f32_e32 v20, v84, v138
	v_sub_f32_e32 v5, v5, v138
; #define ISSUE_L(t, so) do { const unsigned so_ = (unsigned)(so); \
;     if ((t) < NT) { const char* kb_ = Kh + KROWB(t); pg8::glds16_s(kb_, koff[0], ldsK + so_); pg8::glds16_s(kb_, koff[1], ldsK + so_ + 1024u); } \
;     if ((t) >= 1) { const char* vb_ = Vh + KROWB((t) - 1); pg8::glds16_s(vb_, voff[0], ldsV + so_); pg8::glds16_s(vb_, voff[1], ldsV + so_ + 1024u); } } while (0)
; #define PBAR() asm volatile("s_waitcnt lgkmcnt(0)\n\ts_barrier" ::: "memory")
; #define PBAR_V0() asm volatile("s_waitcnt vmcnt(0) lgkmcnt(0)\n\ts_barrier" ::: "memory")
; #define YPH() YSOFT(false)
; #define ISSUE_L(t, sl) do { \
;     if ((t) < NT) pg8::glds16_s(Kh + KROWB(t), koff, ldsK + (unsigned)(sl) * 8192u); \
;     if ((t) >= 1 && (t) <= NT) pg8::glds16_s((const char*)V8 + (size_t)((t) - 1) * 8192, voff, ldsV + (unsigned)(sl) * 8192u); } while (0)
; #define PBAR() asm volatile("s_waitcnt lgkmcnt(0)\n\ts_barrier" ::: "memory")
; #define PBAR_V0() asm volatile("s_waitcnt vmcnt(0) lgkmcnt(0)\n\ts_barrier" ::: "memory")
; #define PBAR_V3() asm volatile("s_waitcnt vmcnt(2) lgkmcnt(0)\n\ts_barrier" ::: "memory")
; #define YPH() YSOFT(false)
; __device__ __forceinline__ void attn_unit_f8(const bf16_t* __restrict__ Q, const bf16_t* __restrict__ Kb, const unsigned char* __restrict__ V8, bf16_t* __restrict__ O, ...
;     ...
;     QKT(0); ISSUE_L(2, si); si = NEXT3(si); PBAR();
;     YSOFT(true); PBAR_V3();
;     for (int t = 1; t < NT; ++t) {
;       __builtin_amdgcn_s_setprio(1); QKT(sx); PV8(sx); sx = NEXT3(sx);
;       if (t + 2 <= NT) { ISSUE_L(t + 2, si); si = NEXT3(si); }
;       __builtin_amdgcn_s_setprio(0);
;       PBAR();
;       YPH(); if (t + 2 < NT) PBAR_V3(); else PBAR_V0();
	v_sub_f32_e32 v21, v85, v138
	v_sub_f32_e32 v8, v8, v138
	v_sub_f32_e32 v24, v88, v138
	v_sub_f32_e32 v9, v9, v138
	v_sub_f32_e32 v25, v89, v138
	v_sub_f32_e32 v12, v12, v138
	v_sub_f32_e32 v30, v92, v138
	v_sub_f32_e32 v13, v13, v138
	v_sub_f32_e32 v31, v93, v138
	v_sub_f32_e32 v16, v16, v138
	v_sub_f32_e32 v34, v96, v138
	v_sub_f32_e32 v17, v17, v138
	v_sub_f32_e32 v35, v97, v138
	v_exp_f32_e32 v4, v4
	v_exp_f32_e32 v5, v5
	v_exp_f32_e32 v8, v8
	v_exp_f32_e32 v9, v9
	v_exp_f32_e32 v12, v12
	v_exp_f32_e32 v13, v13
	v_exp_f32_e32 v16, v16
	v_exp_f32_e32 v17, v17
	v_exp_f32_e32 v20, v20
	v_exp_f32_e32 v21, v21
	v_exp_f32_e32 v24, v24
	v_exp_f32_e32 v25, v25
	v_exp_f32_e32 v30, v30
	v_exp_f32_e32 v31, v31
	v_exp_f32_e32 v34, v34
	v_exp_f32_e32 v35, v35
	v_cvt_pk_fp8_f32 v130, v2, v3
	v_cvt_pk_fp8_f32 v134, v18, v19
	v_cvt_pk_fp8_f32 v131, v6, v7
	v_cvt_pk_fp8_f32 v135, v22, v23
	v_cvt_pk_fp8_f32 v132, v10, v11
	v_cvt_pk_fp8_f32 v136, v28, v29
	v_cvt_pk_fp8_f32 v133, v14, v15
	v_cvt_pk_fp8_f32 v137, v32, v33
	v_xor_b32_e32 v82, 0x80000000, v138
	v_mov_b32_e32 v83, v82
	v_mov_b32_e32 v84, v82
	v_mov_b32_e32 v85, v82
	v_mov_b32_e32 v86, v82
	v_mov_b32_e32 v87, v82
	v_mov_b32_e32 v88, v82
	v_mov_b32_e32 v89, v82
	v_mov_b32_e32 v90, v82
	v_mov_b32_e32 v91, v82
	v_mov_b32_e32 v92, v82
	v_mov_b32_e32 v93, v82
	v_mov_b32_e32 v94, v82
	v_mov_b32_e32 v95, v82
	v_mov_b32_e32 v96, v82
	v_mov_b32_e32 v97, v82
	v_cvt_pk_fp8_f32 v130, v4, v5 op_sel:[0,0,1]
	v_cvt_pk_fp8_f32 v134, v20, v21 op_sel:[0,0,1]
	v_cvt_pk_fp8_f32 v131, v8, v9 op_sel:[0,0,1]
	v_cvt_pk_fp8_f32 v135, v24, v25 op_sel:[0,0,1]
	v_cvt_pk_fp8_f32 v132, v12, v13 op_sel:[0,0,1]
	v_cvt_pk_fp8_f32 v136, v30, v31 op_sel:[0,0,1]
	v_cvt_pk_fp8_f32 v133, v16, v17 op_sel:[0,0,1]
	v_cvt_pk_fp8_f32 v137, v34, v35 op_sel:[0,0,1]
	s_waitcnt vmcnt(2) lgkmcnt(0)
	s_barrier
	v_cmp_gt_u32_e64 s[2:3], 32, v181
	s_setprio 1
	ds_read_b128 v[6:9], v27 offset:32768
	ds_read_b128 v[2:5], v26 offset:32768
	ds_read_b128 v[66:69], v26 offset:36864
	ds_read_b128 v[70:73], v27 offset:36864
	s_or_b32 s0, s84, 0xc0
	s_ashr_i32 s1, s0, 31
	s_waitcnt lgkmcnt(2)
	v_mfma_f32_32x32x64_f8f6f4 v[98:113], v[2:9], v[154:161], v[82:97]
	ds_read_b128 v[6:9], v150 offset:8192
	ds_read_b128 v[2:5], v149 offset:8192
	ds_read_b128 v[18:21], v149 offset:10240
	ds_read_b128 v[22:25], v150 offset:10240
	ds_read_b128 v[38:41], v150 offset:12288
	ds_read_b128 v[34:37], v149 offset:12288
	ds_read_b128 v[50:53], v149 offset:14336
	ds_read_b128 v[54:57], v150 offset:14336
	s_lshl_b64 s[0:1], s[0:1], 10
	s_add_u32 s0, s59, s0
	s_addc_u32 s1, s60, s1
	s_waitcnt lgkmcnt(6)
	v_mfma_f32_32x32x64_f8f6f4 v[2:17], v[130:137], v[2:9], 0
	s_waitcnt lgkmcnt(4)
	v_mfma_f32_32x32x64_f8f6f4 v[18:33], v[130:137], v[18:25], 0
	s_waitcnt lgkmcnt(2)
	v_mfma_f32_32x32x64_f8f6f4 v[34:49], v[130:137], v[34:41], 0
	s_waitcnt lgkmcnt(0)
	v_mfma_f32_32x32x64_f8f6f4 v[50:65], v[130:137], v[50:57], 0
	v_mfma_f32_32x32x64_f8f6f4 v[114:129], v[66:73], v[154:161], v[82:97]
	s_mov_b32 m0, s57
	s_nop 0
	global_load_lds_dwordx4 v148, s[0:1]
	s_add_u32 s0, s82, 0x4000
	s_addc_u32 s1, s83, 0
	s_mov_b32 m0, s58
	s_nop 0
	global_load_lds_dwordx4 v147, s[0:1]
	v_mfma_f32_32x32x64_f8f6f4 v[66:81], v[130:137], v[162:169], 0
	s_setprio 0
	v_max_f32_e32 v142, v99, v99
	v_max_f32_e32 v143, v98, v98
	v_max_f32_e32 v142, v143, v142
	s_nop 12
	v_max3_f32 v143, v100, v101, v115
	v_max3_f32 v142, v142, v114, v116
	v_max3_f32 v142, v142, v117, v102
	v_max3_f32 v143, v143, v104, v105
	v_max3_f32 v142, v142, v103, v118
	v_max3_f32 v143, v143, v120, v121
	v_max3_f32 v142, v142, v119, v106
	v_max3_f32 v143, v143, v108, v109
	v_max3_f32 v142, v142, v107, v122
	v_max3_f32 v143, v143, v124, v125
	v_max3_f32 v142, v142, v123, v110
	v_max3_f32 v143, v143, v112, v113
	v_max3_f32 v142, v142, v111, v126
	v_max3_f32 v143, v143, v128, v129
	v_max3_f32 v142, v142, v127, v143
	v_mov_b32_e32 v143, v142
	s_nop 1
	v_permlane32_swap_b32_e32 v142, v143
	s_waitcnt lgkmcnt(0)
	s_barrier
	v_max_f32_e32 v143, v143, v143
	v_max_f32_e32 v142, v142, v142
	v_max_f32_e32 v142, v142, v143
	v_cmp_lt_f32_e32 vcc, s69, v142
	s_cbranch_vccz .LBB0_1334
	v_add_f32_e32 v82, 0xc0c00000, v142
	v_max_f32_e32 v142, 0, v82
	v_exp_f32_e64 v143, -v142
	v_add_f32_e32 v138, v138, v142
	v_xor_b32_e32 v82, 0x80000000, v138
	v_mov_b32_e32 v83, v82
	v_mov_b32_e32 v84, v82
	v_mov_b32_e32 v85, v82
	v_mov_b32_e32 v86, v82
	v_mov_b32_e32 v87, v82
	v_mov_b32_e32 v88, v82
	v_mov_b32_e32 v89, v82
	v_mov_b32_e32 v90, v82
	v_mov_b32_e32 v91, v82
	v_mov_b32_e32 v92, v82
	v_mov_b32_e32 v93, v82
	v_mov_b32_e32 v94, v82
	v_mov_b32_e32 v95, v82
	v_mov_b32_e32 v96, v82
	v_mov_b32_e32 v97, v82
	v_cmp_gt_f32_e32 vcc, 1.0, v143
	s_cbranch_vccz .LBB0_1333
	s_and_saveexec_b64 s[0:1], s[2:3]
	ds_write_b32 v151, v143 offset:49280
	s_or_b64 exec, exec, s[0:1]
	s_waitcnt lgkmcnt(0)
	v_lshl_add_u32 v143, v141, 2, s66
	ds_read_b128 v[170:173], v143 offset:49376
	ds_read_b128 v[174:177], v143 offset:49344
	ds_read_b128 v[198:201], v143 offset:49312
	ds_read_b128 v[202:205], v143 offset:49280
	s_waitcnt lgkmcnt(3)
	v_pk_mul_f32 v[16:17], v[16:17], v[172:173]
	s_waitcnt lgkmcnt(2)
	v_pk_mul_f32 v[12:13], v[12:13], v[176:177]
	s_waitcnt lgkmcnt(1)
	v_pk_mul_f32 v[8:9], v[8:9], v[200:201]
	s_waitcnt lgkmcnt(0)
	v_pk_mul_f32 v[4:5], v[4:5], v[204:205]
	v_pk_mul_f32 v[14:15], v[14:15], v[170:171]
	v_pk_mul_f32 v[10:11], v[10:11], v[174:175]
	v_pk_mul_f32 v[6:7], v[6:7], v[198:199]
	v_pk_mul_f32 v[2:3], v[2:3], v[202:203]
	v_pk_mul_f32 v[32:33], v[32:33], v[172:173]
	v_pk_mul_f32 v[28:29], v[28:29], v[176:177]
	v_pk_mul_f32 v[24:25], v[24:25], v[200:201]
	v_pk_mul_f32 v[20:21], v[20:21], v[204:205]
	v_pk_mul_f32 v[30:31], v[30:31], v[170:171]
	v_pk_mul_f32 v[26:27], v[26:27], v[174:175]
	v_pk_mul_f32 v[22:23], v[22:23], v[198:199]
	v_pk_mul_f32 v[18:19], v[18:19], v[202:203]
	v_pk_mul_f32 v[48:49], v[48:49], v[172:173]
	v_pk_mul_f32 v[44:45], v[44:45], v[176:177]
	v_pk_mul_f32 v[40:41], v[40:41], v[200:201]
	v_pk_mul_f32 v[36:37], v[36:37], v[204:205]
	v_pk_mul_f32 v[46:47], v[46:47], v[170:171]
	v_pk_mul_f32 v[42:43], v[42:43], v[174:175]
	v_pk_mul_f32 v[38:39], v[38:39], v[198:199]
	v_pk_mul_f32 v[34:35], v[34:35], v[202:203]
	v_pk_mul_f32 v[64:65], v[64:65], v[172:173]
	v_pk_mul_f32 v[60:61], v[60:61], v[176:177]
	v_pk_mul_f32 v[56:57], v[56:57], v[200:201]
	v_pk_mul_f32 v[52:53], v[52:53], v[204:205]
	v_pk_mul_f32 v[62:63], v[62:63], v[170:171]
	v_pk_mul_f32 v[58:59], v[58:59], v[174:175]
	v_pk_mul_f32 v[54:55], v[54:55], v[198:199]
	v_pk_mul_f32 v[50:51], v[50:51], v[202:203]
	v_pk_mul_f32 v[80:81], v[80:81], v[172:173]
	v_pk_mul_f32 v[76:77], v[76:77], v[176:177]
	v_pk_mul_f32 v[72:73], v[72:73], v[200:201]
	v_pk_mul_f32 v[68:69], v[68:69], v[204:205]
	v_pk_mul_f32 v[78:79], v[78:79], v[170:171]
	v_pk_mul_f32 v[74:75], v[74:75], v[174:175]
	v_pk_mul_f32 v[70:71], v[70:71], v[198:199]
	v_pk_mul_f32 v[66:67], v[66:67], v[202:203]

; #define ISSUE_L(t, so) do { const unsigned so_ = (unsigned)(so); \
;     if ((t) < NT) { const char* kb_ = Kh + KROWB(t); pg8::glds16_s(kb_, koff[0], ldsK + so_); pg8::glds16_s(kb_, koff[1], ldsK + so_ + 1024u); } \
;     if ((t) >= 1) { const char* vb_ = Vh + KROWB((t) - 1); pg8::glds16_s(vb_, voff[0], ldsV + so_); pg8::glds16_s(vb_, voff[1], ldsV + so_ + 1024u); } } while (0)
; #define PBAR() asm volatile("s_waitcnt lgkmcnt(0)\n\ts_barrier" ::: "memory")
; #define PBAR_V0() asm volatile("s_waitcnt vmcnt(0) lgkmcnt(0)\n\ts_barrier" ::: "memory")
; #define YPH() YSOFT(false)
; #define ISSUE_L(t, sl) do { \
;     if ((t) < NT) pg8::glds16_s(Kh + KROWB(t), koff, ldsK + (unsigned)(sl) * 8192u); \
;     if ((t) >= 1 && (t) <= NT) pg8::glds16_s((const char*)V8 + (size_t)((t) - 1) * 8192, voff, ldsV + (unsigned)(sl) * 8192u); } while (0)
; #define PBAR() asm volatile("s_waitcnt lgkmcnt(0)\n\ts_barrier" ::: "memory")
; #define PBAR_V0() asm volatile("s_waitcnt vmcnt(0) lgkmcnt(0)\n\ts_barrier" ::: "memory")
; #define PBAR_V3() asm volatile("s_waitcnt vmcnt(2) lgkmcnt(0)\n\ts_barrier" ::: "memory")
; #define YPH() YSOFT(false)
; __device__ __forceinline__ void attn_unit_f8(const bf16_t* __restrict__ Q, const bf16_t* __restrict__ Kb, const unsigned char* __restrict__ V8, bf16_t* __restrict__ O, ...
;     ...
;     for (int t = 1; t < NT; ++t) {
;       __builtin_amdgcn_s_setprio(1); QKT(sx); PV8(sx); sx = NEXT3(sx);
;       if (t + 2 <= NT) { ISSUE_L(t + 2, si); si = NEXT3(si); }
;       __builtin_amdgcn_s_setprio(0);
;       PBAR();
;       YPH(); if (t + 2 < NT) PBAR_V3(); else PBAR_V0();
.LBB0_1338:
	s_setprio 1
	s_lshl_b32 s0, s26, 13
	v_add_u32_e32 v98, s0, v153
	v_add_u32_e32 v123, v98, v140
	v_add_u32_e32 v122, v98, v139
	ds_read_b128 v[102:105], v123 offset:24576
	ds_read_b128 v[98:101], v122 offset:24576
	v_add_u32_e32 v125, s0, v150
	v_add_u32_e32 v124, s0, v149
	v_mfma_f32_32x32x64_f8f6f4 v[66:81], v[130:137], v[162:169], v[66:81]
	s_add_i32 s0, s28, s64
	s_ashr_i32 s1, s0, 31
	s_lshl_b64 s[0:1], s[0:1], 10
	s_add_u32 s0, s59, s0
	s_addc_u32 s1, s60, s1
	s_lshl_b32 s12, s27, 13
	s_add_i32 s13, s12, s57
	s_waitcnt lgkmcnt(0)
	v_mfma_f32_32x32x64_f8f6f4 v[98:113], v[98:105], v[154:161], v[82:97]
	ds_read_b128 v[118:121], v125
	ds_read_b128 v[114:117], v124
	s_waitcnt lgkmcnt(0)
	v_mfma_f32_32x32x64_f8f6f4 v[2:17], v[130:137], v[114:121], v[2:17]
	ds_read_b128 v[114:117], v124 offset:2048
	ds_read_b128 v[118:121], v125 offset:2048
	s_waitcnt lgkmcnt(0)
	v_mfma_f32_32x32x64_f8f6f4 v[18:33], v[130:137], v[114:121], v[18:33]
	ds_read_b128 v[118:121], v125 offset:4096
	ds_read_b128 v[114:117], v124 offset:4096
	s_waitcnt lgkmcnt(0)
	v_mfma_f32_32x32x64_f8f6f4 v[34:49], v[130:137], v[114:121], v[34:49]
	ds_read_b128 v[114:117], v124 offset:6144
	ds_read_b128 v[118:121], v125 offset:6144
	s_waitcnt lgkmcnt(0)
	v_mfma_f32_32x32x64_f8f6f4 v[50:65], v[130:137], v[114:121], v[50:65]
	ds_read_b128 v[114:117], v122 offset:28672
	ds_read_b128 v[118:121], v123 offset:28672
	s_waitcnt lgkmcnt(0)
	v_mfma_f32_32x32x64_f8f6f4 v[114:129], v[114:121], v[154:161], v[82:97]
	s_mov_b32 m0, s13
	s_nop 0
	global_load_lds_dwordx4 v148, s[0:1]
	s_add_u32 s0, s47, 0x2000
	s_addc_u32 s1, s61, 0
	s_add_i32 s12, s12, s58
	s_mov_b32 m0, s12
	s_nop 0
	global_load_lds_dwordx4 v147, s[0:1]
	s_setprio 0
	v_max_f32_e32 v142, v99, v99
	v_max_f32_e32 v143, v98, v98
	v_max_f32_e32 v142, v143, v142
	s_nop 12
	v_max3_f32 v143, v100, v101, v115
	v_max3_f32 v142, v142, v114, v116
	v_max3_f32 v142, v142, v117, v102
	v_max3_f32 v143, v143, v104, v105
	v_max3_f32 v142, v142, v103, v118
	v_max3_f32 v143, v143, v120, v121
	v_max3_f32 v142, v142, v119, v106
	v_max3_f32 v143, v143, v108, v109
	v_max3_f32 v142, v142, v107, v122
	v_max3_f32 v143, v143, v124, v125
	v_max3_f32 v142, v142, v123, v110
	v_max3_f32 v143, v143, v112, v113
	v_max3_f32 v142, v142, v111, v126
	v_max3_f32 v143, v143, v128, v129
	v_max3_f32 v142, v142, v127, v143
	v_mov_b32_e32 v143, v142
	s_nop 1
	v_permlane32_swap_b32_e32 v142, v143
	s_waitcnt lgkmcnt(0)
	s_barrier
	v_max_f32_e32 v143, v143, v143
	v_max_f32_e32 v142, v142, v142
	v_max_f32_e32 v142, v142, v143
	v_cmp_lt_f32_e32 vcc, s69, v142
	s_cbranch_vccz .LBB0_1337
	v_add_f32_e32 v82, 0xc0c00000, v142
	v_max_f32_e32 v142, 0, v82
	v_exp_f32_e64 v143, -v142
	v_add_f32_e32 v138, v138, v142
	v_xor_b32_e32 v82, 0x80000000, v138
	v_mov_b32_e32 v83, v82
	v_mov_b32_e32 v84, v82
	v_mov_b32_e32 v85, v82
	v_mov_b32_e32 v86, v82
	v_mov_b32_e32 v87, v82
	v_mov_b32_e32 v88, v82
	v_mov_b32_e32 v89, v82
	v_mov_b32_e32 v90, v82
	v_mov_b32_e32 v91, v82
	v_mov_b32_e32 v92, v82
	v_mov_b32_e32 v93, v82
	v_mov_b32_e32 v94, v82
	v_mov_b32_e32 v95, v82
	v_mov_b32_e32 v96, v82
	v_mov_b32_e32 v97, v82
	v_cmp_gt_f32_e32 vcc, 1.0, v143
	s_cbranch_vccz .LBB0_1336
	s_and_saveexec_b64 s[0:1], s[2:3]
	s_cbranch_execz .LBB0_1335
	ds_write_b32 v151, v143 offset:49280
	s_branch .LBB0_1335
; #define ISSUE_L(t, so) do { const unsigned so_ = (unsigned)(so); \
;     if ((t) < NT) { const char* kb_ = Kh + KROWB(t); pg8::glds16_s(kb_, koff[0], ldsK + so_); pg8::glds16_s(kb_, koff[1], ldsK + so_ + 1024u); } \
;     if ((t) >= 1) { const char* vb_ = Vh + KROWB((t) - 1); pg8::glds16_s(vb_, voff[0], ldsV + so_); pg8::glds16_s(vb_, voff[1], ldsV + so_ + 1024u); } } while (0)
; #define PBAR() asm volatile("s_waitcnt lgkmcnt(0)\n\ts_barrier" ::: "memory")
; #define PBAR_V0() asm volatile("s_waitcnt vmcnt(0) lgkmcnt(0)\n\ts_barrier" ::: "memory")
; #define YPH() YSOFT(false)
; #define ISSUE_L(t, sl) do { \
;     if ((t) < NT) pg8::glds16_s(Kh + KROWB(t), koff, ldsK + (unsigned)(sl) * 8192u); \
;     if ((t) >= 1 && (t) <= NT) pg8::glds16_s((const char*)V8 + (size_t)((t) - 1) * 8192, voff, ldsV + (unsigned)(sl) * 8192u); } while (0)
; #define PBAR() asm volatile("s_waitcnt lgkmcnt(0)\n\ts_barrier" ::: "memory")
; #define PBAR_V0() asm volatile("s_waitcnt vmcnt(0) lgkmcnt(0)\n\ts_barrier" ::: "memory")
; #define PBAR_V3() asm volatile("s_waitcnt vmcnt(2) lgkmcnt(0)\n\ts_barrier" ::: "memory")
; #define YPH() YSOFT(false)
; __device__ __forceinline__ void attn_unit_f8(const bf16_t* __restrict__ Q, const bf16_t* __restrict__ Kb, const unsigned char* __restrict__ V8, bf16_t* __restrict__ O, ...
;     ...
;   f32x16 p0, p1; i32x8 p8 = i32x8{};
;   i32x8 onesf = (i32x8){0x38383838, 0x38383838, 0x38383838, 0x38383838, 0x38383838, 0x38383838, 0x38383838, 0x38383838}; asm volatile("" : "+v"(onesf));
;   f32x16 negm = f32x16{}; asm volatile("" : "+v"(negm));
;   const int scl1 = 0x7F7F7F7F;
;     ...
;     for (int t = 1; t < NT; ++t) {
;       __builtin_amdgcn_s_setprio(1); QKT(sx); PV8(sx); sx = NEXT3(sx);
;       if (t + 2 <= NT) { ISSUE_L(t + 2, si); si = NEXT3(si); }
;       __builtin_amdgcn_s_setprio(0);
;       PBAR();
;       YPH(); if (t + 2 < NT) PBAR_V3(); else PBAR_V0();
.LBB0_1342:
	s_setprio 1
	s_lshl_b32 s0, s26, 13
	s_add_i32 s1, s0, 0
	v_add_u32_e32 v98, s1, v152
	v_add_u32_e32 v123, v98, v140
	v_add_u32_e32 v122, v98, v139
	ds_read_b128 v[102:105], v123 offset:24576
	ds_read_b128 v[98:101], v122 offset:24576
	v_add_u32_e32 v125, s0, v150
	v_add_u32_e32 v124, s0, v149
	v_mfma_f32_32x32x64_f8f6f4 v[66:81], v[130:137], v[162:169], v[66:81]
	s_lshl_b32 s12, s27, 13
	s_add_u32 s0, s82, 0x106000
	s_addc_u32 s1, s83, 0
	s_add_i32 s12, s12, s58
	s_waitcnt lgkmcnt(0)
	v_mfma_f32_32x32x64_f8f6f4 v[98:113], v[98:105], v[154:161], v[82:97]
	ds_read_b128 v[118:121], v125
	ds_read_b128 v[114:117], v124
	s_waitcnt lgkmcnt(0)
	v_mfma_f32_32x32x64_f8f6f4 v[2:17], v[130:137], v[114:121], v[2:17]
	ds_read_b128 v[114:117], v124 offset:2048
	ds_read_b128 v[118:121], v125 offset:2048
	s_waitcnt lgkmcnt(0)
	v_mfma_f32_32x32x64_f8f6f4 v[18:33], v[130:137], v[114:121], v[18:33]
	ds_read_b128 v[118:121], v125 offset:4096
	ds_read_b128 v[114:117], v124 offset:4096
	s_waitcnt lgkmcnt(0)
	v_mfma_f32_32x32x64_f8f6f4 v[34:49], v[130:137], v[114:121], v[34:49]
	ds_read_b128 v[114:117], v124 offset:6144
	ds_read_b128 v[118:121], v125 offset:6144
	s_waitcnt lgkmcnt(0)
	v_mfma_f32_32x32x64_f8f6f4 v[50:65], v[130:137], v[114:121], v[50:65]
	ds_read_b128 v[114:117], v122 offset:28672
	ds_read_b128 v[118:121], v123 offset:28672
	s_waitcnt lgkmcnt(0)
	v_mfma_f32_32x32x64_f8f6f4 v[114:129], v[114:121], v[154:161], v[82:97]
	s_mov_b32 m0, s12
	s_nop 0
	global_load_lds_dwordx4 v147, s[0:1]
	s_setprio 0
	v_max_f32_e32 v142, v99, v99
	v_max_f32_e32 v143, v98, v98
	v_max_f32_e32 v142, v143, v142
	s_nop 15
	v_max3_f32 v143, v100, v101, v115
	v_max3_f32 v142, v142, v114, v116
	v_max3_f32 v142, v142, v117, v102
	v_max3_f32 v143, v143, v104, v105
	v_max3_f32 v142, v142, v103, v118
	v_max3_f32 v143, v143, v120, v121
	v_max3_f32 v142, v142, v119, v106
	v_max3_f32 v143, v143, v108, v109
	v_max3_f32 v142, v142, v107, v122
	v_max3_f32 v143, v143, v124, v125
	v_max3_f32 v142, v142, v123, v110
	v_max3_f32 v143, v143, v112, v113
	v_max3_f32 v142, v142, v111, v126
	v_max3_f32 v143, v143, v128, v129
	v_max3_f32 v142, v142, v127, v143
	v_mov_b32_e32 v143, v142
	s_nop 1
	v_permlane32_swap_b32_e32 v142, v143
	s_waitcnt lgkmcnt(0)
	s_barrier
	v_max_f32_e32 v143, v143, v143
	v_max_f32_e32 v142, v142, v142
	v_max_f32_e32 v142, v142, v143
	v_cmp_lt_f32_e32 vcc, s69, v142
	s_cbranch_vccz .LBB0_1348
	v_add_f32_e32 v82, 0xc0c00000, v142
	v_max_f32_e32 v142, 0, v82
	v_exp_f32_e64 v143, -v142
	v_add_f32_e32 v138, v138, v142
	v_xor_b32_e32 v82, 0x80000000, v138
	v_mov_b32_e32 v83, v82
	v_mov_b32_e32 v84, v82
	v_mov_b32_e32 v85, v82
	v_mov_b32_e32 v86, v82
	v_mov_b32_e32 v87, v82
	v_mov_b32_e32 v88, v82
	v_mov_b32_e32 v89, v82
	v_mov_b32_e32 v90, v82
	v_mov_b32_e32 v91, v82
	v_mov_b32_e32 v92, v82
	v_mov_b32_e32 v93, v82
	v_mov_b32_e32 v94, v82
	v_mov_b32_e32 v95, v82
	v_mov_b32_e32 v96, v82
	v_mov_b32_e32 v97, v82
	v_cmp_gt_f32_e32 vcc, 1.0, v143
	s_cbranch_vccz .LBB0_1347
	s_and_saveexec_b64 s[0:1], s[2:3]
	ds_write_b32 v151, v143 offset:49280
	s_or_b64 exec, exec, s[0:1]
	s_waitcnt lgkmcnt(0)
	ds_read_b128 v[170:173], v141 offset:49376
	ds_read_b128 v[174:177], v141 offset:49344
	ds_read_b128 v[198:201], v141 offset:49312
	ds_read_b128 v[202:205], v141 offset:49280
	s_waitcnt lgkmcnt(3)
	v_pk_mul_f32 v[16:17], v[16:17], v[172:173]
	s_waitcnt lgkmcnt(2)
	v_pk_mul_f32 v[12:13], v[12:13], v[176:177]
	s_waitcnt lgkmcnt(1)
	v_pk_mul_f32 v[8:9], v[8:9], v[200:201]
	s_waitcnt lgkmcnt(0)
	v_pk_mul_f32 v[4:5], v[4:5], v[204:205]
	v_pk_mul_f32 v[14:15], v[14:15], v[170:171]
	v_pk_mul_f32 v[10:11], v[10:11], v[174:175]
	v_pk_mul_f32 v[6:7], v[6:7], v[198:199]
	v_pk_mul_f32 v[2:3], v[2:3], v[202:203]
	v_pk_mul_f32 v[32:33], v[32:33], v[172:173]
	v_pk_mul_f32 v[28:29], v[28:29], v[176:177]
	v_pk_mul_f32 v[24:25], v[24:25], v[200:201]
	v_pk_mul_f32 v[20:21], v[20:21], v[204:205]
	v_pk_mul_f32 v[30:31], v[30:31], v[170:171]
	v_pk_mul_f32 v[26:27], v[26:27], v[174:175]
	v_pk_mul_f32 v[22:23], v[22:23], v[198:199]
	v_pk_mul_f32 v[18:19], v[18:19], v[202:203]
	v_pk_mul_f32 v[48:49], v[48:49], v[172:173]
	v_pk_mul_f32 v[44:45], v[44:45], v[176:177]
	v_pk_mul_f32 v[40:41], v[40:41], v[200:201]
	v_pk_mul_f32 v[36:37], v[36:37], v[204:205]
	v_pk_mul_f32 v[46:47], v[46:47], v[170:171]
	v_pk_mul_f32 v[42:43], v[42:43], v[174:175]
	v_pk_mul_f32 v[38:39], v[38:39], v[198:199]
	v_pk_mul_f32 v[34:35], v[34:35], v[202:203]
	v_pk_mul_f32 v[64:65], v[64:65], v[172:173]
	v_pk_mul_f32 v[60:61], v[60:61], v[176:177]
	v_pk_mul_f32 v[56:57], v[56:57], v[200:201]
	v_pk_mul_f32 v[52:53], v[52:53], v[204:205]
	v_pk_mul_f32 v[62:63], v[62:63], v[170:171]
	v_pk_mul_f32 v[58:59], v[58:59], v[174:175]
	v_pk_mul_f32 v[54:55], v[54:55], v[198:199]
	v_pk_mul_f32 v[50:51], v[50:51], v[202:203]
	v_pk_mul_f32 v[80:81], v[80:81], v[172:173]
	v_pk_mul_f32 v[76:77], v[76:77], v[176:177]
	v_pk_mul_f32 v[72:73], v[72:73], v[200:201]
	v_pk_mul_f32 v[68:69], v[68:69], v[204:205]
	v_pk_mul_f32 v[78:79], v[78:79], v[170:171]
	v_pk_mul_f32 v[74:75], v[74:75], v[174:175]
	v_pk_mul_f32 v[70:71], v[70:71], v[198:199]
	v_pk_mul_f32 v[66:67], v[66:67], v[202:203]

; #define ISSUE_L(t, so) do { const unsigned so_ = (unsigned)(so); \
;     if ((t) < NT) { const char* kb_ = Kh + KROWB(t); pg8::glds16_s(kb_, koff[0], ldsK + so_); pg8::glds16_s(kb_, koff[1], ldsK + so_ + 1024u); } \
;     if ((t) >= 1) { const char* vb_ = Vh + KROWB((t) - 1); pg8::glds16_s(vb_, voff[0], ldsV + so_); pg8::glds16_s(vb_, voff[1], ldsV + so_ + 1024u); } } while (0)
; #define PBAR() asm volatile("s_waitcnt lgkmcnt(0)\n\ts_barrier" ::: "memory")
; #define PBAR_V0() asm volatile("s_waitcnt vmcnt(0) lgkmcnt(0)\n\ts_barrier" ::: "memory")
; #define YPH() YSOFT(false)
; #define ISSUE_L(t, sl) do { \
;     if ((t) < NT) pg8::glds16_s(Kh + KROWB(t), koff, ldsK + (unsigned)(sl) * 8192u); \
;     if ((t) >= 1 && (t) <= NT) pg8::glds16_s((const char*)V8 + (size_t)((t) - 1) * 8192, voff, ldsV + (unsigned)(sl) * 8192u); } while (0)
; #define PBAR() asm volatile("s_waitcnt lgkmcnt(0)\n\ts_barrier" ::: "memory")
; #define PBAR_V0() asm volatile("s_waitcnt vmcnt(0) lgkmcnt(0)\n\ts_barrier" ::: "memory")
; #define PBAR_V3() asm volatile("s_waitcnt vmcnt(2) lgkmcnt(0)\n\ts_barrier" ::: "memory")
; #define YPH() YSOFT(false)
; __device__ __forceinline__ void attn_unit_f8(const bf16_t* __restrict__ Q, const bf16_t* __restrict__ Kb, const unsigned char* __restrict__ V8, bf16_t* __restrict__ O, ...
;     ...
;   f32x16 p0, p1; i32x8 p8 = i32x8{};
;   i32x8 onesf = (i32x8){0x38383838, 0x38383838, 0x38383838, 0x38383838, 0x38383838, 0x38383838, 0x38383838, 0x38383838}; asm volatile("" : "+v"(onesf));
;   f32x16 negm = f32x16{}; asm volatile("" : "+v"(negm));
;   const int scl1 = 0x7F7F7F7F;
;     ...
;     for (int t = 1; t < NT; ++t) {
;       __builtin_amdgcn_s_setprio(1); QKT(sx); PV8(sx); sx = NEXT3(sx);
;       if (t + 2 <= NT) { ISSUE_L(t + 2, si); si = NEXT3(si); }
;       __builtin_amdgcn_s_setprio(0);
;       PBAR();
;       YPH(); if (t + 2 < NT) PBAR_V3(); else PBAR_V0();
;     }
;     PV8(sx); PBAR();
.LBB0_1348:
	v_exp_f32_e32 v98, v98
	v_exp_f32_e32 v99, v99
	v_exp_f32_e32 v102, v102
	v_exp_f32_e32 v103, v103
	v_exp_f32_e32 v106, v106
	v_exp_f32_e32 v107, v107
	v_exp_f32_e32 v110, v110
	v_exp_f32_e32 v111, v111
	v_exp_f32_e32 v114, v114
	v_exp_f32_e32 v115, v115
	v_exp_f32_e32 v118, v118
	v_exp_f32_e32 v119, v119
	v_exp_f32_e32 v122, v122
	v_exp_f32_e32 v123, v123
	v_exp_f32_e32 v126, v126
	v_exp_f32_e32 v127, v127
	v_exp_f32_e32 v100, v100
	v_exp_f32_e32 v101, v101
	v_exp_f32_e32 v104, v104
	v_exp_f32_e32 v105, v105
	v_exp_f32_e32 v108, v108
	v_exp_f32_e32 v109, v109
	v_exp_f32_e32 v112, v112
	v_exp_f32_e32 v113, v113
	v_exp_f32_e32 v116, v116
	v_exp_f32_e32 v117, v117
	v_exp_f32_e32 v120, v120
	v_exp_f32_e32 v121, v121
	v_exp_f32_e32 v124, v124
	v_exp_f32_e32 v125, v125
	v_exp_f32_e32 v128, v128
	v_exp_f32_e32 v129, v129
	v_cvt_pk_fp8_f32 v130, v98, v99
	v_cvt_pk_fp8_f32 v134, v114, v115
	v_cvt_pk_fp8_f32 v131, v102, v103
	v_cvt_pk_fp8_f32 v135, v118, v119
	v_cvt_pk_fp8_f32 v132, v106, v107
	v_cvt_pk_fp8_f32 v136, v122, v123
	v_cvt_pk_fp8_f32 v133, v110, v111
	v_cvt_pk_fp8_f32 v137, v126, v127
	v_cvt_pk_fp8_f32 v130, v100, v101 op_sel:[0,0,1]
	v_cvt_pk_fp8_f32 v134, v116, v117 op_sel:[0,0,1]
	v_cvt_pk_fp8_f32 v131, v104, v105 op_sel:[0,0,1]
	v_cvt_pk_fp8_f32 v135, v120, v121 op_sel:[0,0,1]
	v_cvt_pk_fp8_f32 v132, v108, v109 op_sel:[0,0,1]
	v_cvt_pk_fp8_f32 v136, v124, v125 op_sel:[0,0,1]
	v_cvt_pk_fp8_f32 v133, v112, v113 op_sel:[0,0,1]
	v_cvt_pk_fp8_f32 v137, v128, v129 op_sel:[0,0,1]
	s_add_i32 s0, s26, 1
	s_waitcnt vmcnt(0) lgkmcnt(0)
	s_barrier
	s_cmp_lg_u32 s26, 2
	s_cselect_b32 s26, s0, 0
	s_setprio 1
	s_lshl_b32 s27, s26, 13
	s_add_i32 s0, s27, 0
	v_add_u32_e32 v98, s0, v152
	v_add_u32_e32 v123, v98, v140
	v_add_u32_e32 v122, v98, v139
	ds_read_b128 v[102:105], v123 offset:24576
	ds_read_b128 v[98:101], v122 offset:24576
	v_add_u32_e32 v125, s27, v150
	v_add_u32_e32 v124, s27, v149
	v_mfma_f32_32x32x64_f8f6f4 v[66:81], v[130:137], v[162:169], v[66:81]
	s_waitcnt lgkmcnt(0)
	v_mfma_f32_32x32x64_f8f6f4 v[98:113], v[98:105], v[154:161], v[82:97]
	ds_read_b128 v[118:121], v125
	ds_read_b128 v[114:117], v124
	s_waitcnt lgkmcnt(0)
	v_mfma_f32_32x32x64_f8f6f4 v[2:17], v[130:137], v[114:121], v[2:17]
	ds_read_b128 v[114:117], v124 offset:2048
	ds_read_b128 v[118:121], v125 offset:2048
	s_waitcnt lgkmcnt(0)
	v_mfma_f32_32x32x64_f8f6f4 v[18:33], v[130:137], v[114:121], v[18:33]
	ds_read_b128 v[118:121], v125 offset:4096
	ds_read_b128 v[114:117], v124 offset:4096
	s_waitcnt lgkmcnt(0)
	v_mfma_f32_32x32x64_f8f6f4 v[34:49], v[130:137], v[114:121], v[34:49]
	ds_read_b128 v[114:117], v124 offset:6144
	ds_read_b128 v[118:121], v125 offset:6144
	s_waitcnt lgkmcnt(0)
	v_mfma_f32_32x32x64_f8f6f4 v[50:65], v[130:137], v[114:121], v[50:65]
	ds_read_b128 v[114:117], v122 offset:28672
	ds_read_b128 v[118:121], v123 offset:28672
	s_waitcnt lgkmcnt(0)
	v_mfma_f32_32x32x64_f8f6f4 v[82:97], v[114:121], v[154:161], v[82:97]
	s_setprio 0
	v_max_f32_e32 v114, v99, v99
	v_max_f32_e32 v115, v98, v98
	v_max_f32_e32 v114, v115, v114
	s_nop 15
	v_max3_f32 v115, v100, v101, v83
	v_max3_f32 v114, v114, v82, v84
	v_max3_f32 v114, v114, v85, v102
	v_max3_f32 v115, v115, v104, v105
	v_max3_f32 v114, v114, v103, v86
	v_max3_f32 v115, v115, v88, v89
	v_max3_f32 v114, v114, v87, v106
	v_max3_f32 v115, v115, v108, v109
	v_max3_f32 v114, v114, v107, v90
	v_max3_f32 v115, v115, v92, v93
	v_max3_f32 v114, v114, v91, v110
	v_max3_f32 v115, v115, v112, v113
	v_max3_f32 v114, v114, v111, v94
	v_max3_f32 v115, v115, v96, v97
	v_max3_f32 v114, v114, v95, v115
	v_mov_b32_e32 v115, v114
	s_nop 1
	v_permlane32_swap_b32_e32 v114, v115
	s_waitcnt lgkmcnt(0)
	s_barrier
	v_max_f32_e32 v115, v115, v115
	v_max_f32_e32 v114, v114, v114
	v_max_f32_e32 v114, v114, v115
	v_cmp_lt_f32_e32 vcc, s69, v114
	s_cbranch_vccz .LBB0_1354
	v_add_f32_e32 v114, 0xc0c00000, v114
	v_max_f32_e32 v139, 0, v114
	v_add_f32_e32 v114, v138, v139
	v_xor_b32_e32 v114, 0x80000000, v114
	v_mov_b32_e32 v115, v114
	v_mov_b32_e32 v116, v114
	v_mov_b32_e32 v117, v114
	v_mov_b32_e32 v118, v114
	v_mov_b32_e32 v119, v114
	v_mov_b32_e32 v120, v114
	v_mov_b32_e32 v121, v114
	v_mov_b32_e32 v122, v114
	v_mov_b32_e32 v123, v114
	v_mov_b32_e32 v124, v114
	v_mov_b32_e32 v125, v114
	v_mov_b32_e32 v126, v114
	v_mov_b32_e32 v127, v114
	v_mov_b32_e32 v128, v114
	v_mov_b32_e32 v129, v114
	s_nop 0
	v_exp_f32_e64 v114, -v139
	s_nop 0
	v_cmp_gt_f32_e32 vcc, 1.0, v114
	s_cbranch_vccz .LBB0_1353
	s_and_saveexec_b64 s[0:1], s[2:3]
	ds_write_b32 v151, v114 offset:49280
	s_or_b64 exec, exec, s[0:1]
	s_waitcnt lgkmcnt(0)
	ds_read_b128 v[114:117], v141 offset:49376
	ds_read_b128 v[118:121], v141 offset:49344
	ds_read_b128 v[122:125], v141 offset:49312
	ds_read_b128 v[126:129], v141 offset:49280
	s_waitcnt lgkmcnt(3)
	v_pk_mul_f32 v[16:17], v[16:17], v[116:117]
	s_waitcnt lgkmcnt(2)
	v_pk_mul_f32 v[12:13], v[12:13], v[120:121]
	s_waitcnt lgkmcnt(1)
	v_pk_mul_f32 v[8:9], v[8:9], v[124:125]
	s_waitcnt lgkmcnt(0)
	v_pk_mul_f32 v[4:5], v[4:5], v[128:129]
	v_pk_mul_f32 v[14:15], v[14:15], v[114:115]
	v_pk_mul_f32 v[10:11], v[10:11], v[118:119]
	v_pk_mul_f32 v[6:7], v[6:7], v[122:123]
	v_pk_mul_f32 v[2:3], v[2:3], v[126:127]
	v_pk_mul_f32 v[32:33], v[32:33], v[116:117]
	v_pk_mul_f32 v[28:29], v[28:29], v[120:121]
	v_pk_mul_f32 v[24:25], v[24:25], v[124:125]
	v_pk_mul_f32 v[20:21], v[20:21], v[128:129]
	v_pk_mul_f32 v[30:31], v[30:31], v[114:115]
	v_pk_mul_f32 v[26:27], v[26:27], v[118:119]
	v_pk_mul_f32 v[22:23], v[22:23], v[122:123]
	v_pk_mul_f32 v[18:19], v[18:19], v[126:127]
	v_pk_mul_f32 v[48:49], v[48:49], v[116:117]
	v_pk_mul_f32 v[44:45], v[44:45], v[120:121]
	v_pk_mul_f32 v[40:41], v[40:41], v[124:125]
	v_pk_mul_f32 v[36:37], v[36:37], v[128:129]
	v_pk_mul_f32 v[46:47], v[46:47], v[114:115]
	v_pk_mul_f32 v[42:43], v[42:43], v[118:119]
	v_pk_mul_f32 v[38:39], v[38:39], v[122:123]
	v_pk_mul_f32 v[34:35], v[34:35], v[126:127]
	v_pk_mul_f32 v[64:65], v[64:65], v[116:117]
	v_pk_mul_f32 v[60:61], v[60:61], v[120:121]
	v_pk_mul_f32 v[56:57], v[56:57], v[124:125]
	v_pk_mul_f32 v[52:53], v[52:53], v[128:129]
	v_pk_mul_f32 v[62:63], v[62:63], v[114:115]
	v_pk_mul_f32 v[58:59], v[58:59], v[118:119]
	v_pk_mul_f32 v[54:55], v[54:55], v[122:123]
	v_pk_mul_f32 v[50:51], v[50:51], v[126:127]
	v_pk_mul_f32 v[80:81], v[80:81], v[116:117]
	v_pk_mul_f32 v[76:77], v[76:77], v[120:121]
	v_pk_mul_f32 v[72:73], v[72:73], v[124:125]
	v_pk_mul_f32 v[68:69], v[68:69], v[128:129]
	v_pk_mul_f32 v[78:79], v[78:79], v[114:115]
	v_pk_mul_f32 v[74:75], v[74:75], v[118:119]
	v_pk_mul_f32 v[70:71], v[70:71], v[122:123]
	v_pk_mul_f32 v[66:67], v[66:67], v[126:127]

; #define PBAR() asm volatile("s_waitcnt lgkmcnt(0)\n\ts_barrier" ::: "memory")
; #define PBAR_V0() asm volatile("s_waitcnt vmcnt(0) lgkmcnt(0)\n\ts_barrier" ::: "memory")
; #define YPH() YSOFT(false)
; #define PBAR() asm volatile("s_waitcnt lgkmcnt(0)\n\ts_barrier" ::: "memory")
; #define PBAR_V0() asm volatile("s_waitcnt vmcnt(0) lgkmcnt(0)\n\ts_barrier" ::: "memory")
; #define PBAR_V3() asm volatile("s_waitcnt vmcnt(2) lgkmcnt(0)\n\ts_barrier" ::: "memory")
; #define YPH() YSOFT(false)
; __device__ __forceinline__ void attn_unit_f8(const bf16_t* __restrict__ Q, const bf16_t* __restrict__ Kb, const unsigned char* __restrict__ V8, bf16_t* __restrict__ O, ...
;     ...
;       YPH(); if (t + 2 < NT) PBAR_V3(); else PBAR_V0();
;     }
;     PV8(sx); PBAR();
;     PBAR();
.LBB0_1354:
	v_exp_f32_e32 v98, v98
	v_exp_f32_e32 v99, v99
	v_exp_f32_e32 v102, v102
	v_exp_f32_e32 v103, v103
	v_exp_f32_e32 v106, v106
	v_exp_f32_e32 v107, v107
	v_exp_f32_e32 v110, v110
	v_exp_f32_e32 v111, v111
	v_exp_f32_e32 v82, v82
	v_exp_f32_e32 v83, v83
	v_exp_f32_e32 v86, v86
	v_exp_f32_e32 v87, v87
	v_exp_f32_e32 v90, v90
	v_exp_f32_e32 v91, v91
	v_exp_f32_e32 v94, v94
	v_exp_f32_e32 v95, v95
	v_exp_f32_e32 v100, v100
	v_exp_f32_e32 v101, v101
	v_exp_f32_e32 v104, v104
	v_exp_f32_e32 v105, v105
	v_exp_f32_e32 v108, v108
	v_exp_f32_e32 v109, v109
	v_exp_f32_e32 v112, v112
	v_exp_f32_e32 v113, v113
	v_exp_f32_e32 v84, v84
	v_exp_f32_e32 v85, v85
	v_exp_f32_e32 v88, v88
	v_exp_f32_e32 v89, v89
	v_exp_f32_e32 v92, v92
	v_exp_f32_e32 v93, v93
	v_exp_f32_e32 v96, v96
	v_exp_f32_e32 v97, v97
	v_cvt_pk_fp8_f32 v130, v98, v99
	v_cvt_pk_fp8_f32 v134, v82, v83
	v_cvt_pk_fp8_f32 v131, v102, v103
	v_cvt_pk_fp8_f32 v135, v86, v87
	v_cvt_pk_fp8_f32 v132, v106, v107
	v_cvt_pk_fp8_f32 v136, v90, v91
	v_cvt_pk_fp8_f32 v133, v110, v111
	v_cvt_pk_fp8_f32 v137, v94, v95
	s_addk_i32 s27, 0x2000
	v_cvt_pk_fp8_f32 v130, v100, v101 op_sel:[0,0,1]
	v_cvt_pk_fp8_f32 v134, v84, v85 op_sel:[0,0,1]
	v_cvt_pk_fp8_f32 v131, v104, v105 op_sel:[0,0,1]
	v_cvt_pk_fp8_f32 v135, v88, v89 op_sel:[0,0,1]
	v_cvt_pk_fp8_f32 v132, v108, v109 op_sel:[0,0,1]
	v_cvt_pk_fp8_f32 v136, v92, v93 op_sel:[0,0,1]
	v_cvt_pk_fp8_f32 v133, v112, v113 op_sel:[0,0,1]
	v_cvt_pk_fp8_f32 v137, v96, v97 op_sel:[0,0,1]
	s_cmp_lg_u32 s26, 2
	s_cselect_b32 s0, s27, 0
	s_waitcnt vmcnt(0) lgkmcnt(0)
	s_barrier
	v_add_u32_e32 v99, s0, v150
	v_add_u32_e32 v98, s0, v149
	ds_read_b128 v[86:89], v99
	ds_read_b128 v[82:85], v98
	ds_read_b128 v[90:93], v98 offset:2048
	ds_read_b128 v[94:97], v99 offset:2048
	s_waitcnt lgkmcnt(2)
	v_mfma_f32_32x32x64_f8f6f4 v[2:17], v[130:137], v[82:89], v[2:17]
	s_waitcnt lgkmcnt(0)
	v_mfma_f32_32x32x64_f8f6f4 v[18:33], v[130:137], v[90:97], v[18:33]
	ds_read_b128 v[86:89], v99 offset:4096
	ds_read_b128 v[82:85], v98 offset:4096
	ds_read_b128 v[90:93], v98 offset:6144
	ds_read_b128 v[94:97], v99 offset:6144
	s_waitcnt lgkmcnt(0)
	s_barrier
	s_waitcnt lgkmcnt(0)
	s_barrier
	s_waitcnt lgkmcnt(2)
	v_mfma_f32_32x32x64_f8f6f4 v[34:49], v[130:137], v[82:89], v[34:49]
	s_waitcnt lgkmcnt(0)
	v_mfma_f32_32x32x64_f8f6f4 v[50:65], v[130:137], v[90:97], v[50:65]
	v_mfma_f32_32x32x64_f8f6f4 v[66:81], v[130:137], v[162:169], v[66:81]
